# prep gate blocks: all x-row loads (both halves) issued up front in new VGPRs, counted waits re-derived; 3 waves per SIMD
# baseline (speedup 1.0000x reference)
.LBB13_3:
	s_cmpk_lt_i32 s2, 0x500
	v_lshrrev_b32_e32 v1, 6, v0
	v_and_b32_e32 v36, 63, v0
	s_cbranch_scc0 .LBB13_5
	v_bfe_u32 v13, v0, 4, 2
	v_and_b32_e32 v12, 15, v0
	s_lshl_b32 s22, s2, 4
	v_lshlrev_b32_e32 v2, 3, v13
	v_lshl_or_b32 v14, v1, 8, v2
	v_or_b32_e32 v2, s22, v12
	s_load_dwordx8 s[4:11], s[0:1], 0x30
	s_load_dwordx2 s[26:27], s[0:1], 0x60
	v_ashrrev_i32_e32 v3, 31, v2
	v_lshlrev_b64 v[2:3], 12, v[2:3]
	s_waitcnt lgkmcnt(0)
	v_lshl_add_u64 v[2:3], s[20:21], 0, v[2:3]
	v_lshlrev_b32_e32 v18, 2, v14
	v_mov_b32_e32 v19, 0
	v_lshl_or_b32 v14, v14, 4, v12
	v_lshl_add_u64 v[10:11], v[2:3], 0, v[18:19]
	v_subrev_u32_e32 v108, s20, v10
	v_lshrrev_b32_e32 v108, 1, v108
	global_load_dwordx4 v[116:119], v[10:11], off offset:528
	global_load_dwordx4 v[112:115], v[10:11], off offset:512
	global_load_dwordx4 v[124:127], v[10:11], off offset:656
	global_load_dwordx4 v[120:123], v[10:11], off offset:640
	global_load_dwordx4 v[132:135], v[10:11], off offset:784
	global_load_dwordx4 v[128:131], v[10:11], off offset:768
	global_load_dwordx4 v[140:143], v[10:11], off offset:912
	global_load_dwordx4 v[136:139], v[10:11], off offset:896
	global_load_dwordx4 v[148:151], v[10:11], off offset:400
	global_load_dwordx4 v[144:147], v[10:11], off offset:384
	v_or_b32_e32 v18, 0x200, v14
	v_lshlrev_b64 v[16:17], 2, v[18:19]
	v_lshlrev_b32_e32 v15, 2, v14
	v_lshl_add_u64 v[28:29], s[4:5], 0, v[16:17]
	v_lshl_add_u64 v[16:17], s[10:11], 0, v[16:17]
	v_or_b32_e32 v18, 0x400, v14
	global_load_dwordx4 v[2:5], v[10:11], off offset:16
	global_load_dwordx4 v[6:9], v[10:11], off
	global_load_dword v37, v15, s[4:5]
	global_load_dword v48, v15, s[10:11]
	global_load_dword v49, v15, s[4:5] offset:64
	global_load_dword v50, v15, s[10:11] offset:64
	global_load_dword v51, v15, s[4:5] offset:128
	global_load_dword v52, v15, s[10:11] offset:128
	global_load_dword v53, v15, s[4:5] offset:192
	global_load_dword v54, v15, s[10:11] offset:192
	global_load_dword v55, v15, s[4:5] offset:256
	global_load_dword v56, v15, s[10:11] offset:256
	global_load_dword v57, v15, s[4:5] offset:320
	global_load_dword v58, v15, s[10:11] offset:320
	global_load_dword v59, v15, s[4:5] offset:384
	global_load_dword v60, v15, s[10:11] offset:384
	global_load_dword v61, v15, s[4:5] offset:448
	global_load_dword v62, v15, s[10:11] offset:448
	global_load_dwordx4 v[20:23], v[10:11], off offset:144
	global_load_dwordx4 v[24:27], v[10:11], off offset:128
	global_load_dword v63, v[28:29], off
	global_load_dword v64, v[16:17], off
	global_load_dword v65, v15, s[4:5] offset:2112
	global_load_dword v66, v15, s[10:11] offset:2112
	global_load_dword v67, v15, s[4:5] offset:2176
	global_load_dword v68, v15, s[10:11] offset:2176
	global_load_dword v69, v15, s[4:5] offset:2240
	global_load_dword v70, v15, s[10:11] offset:2240
	global_load_dword v71, v15, s[4:5] offset:2304
	global_load_dword v72, v15, s[10:11] offset:2304
	global_load_dword v73, v15, s[4:5] offset:2368
	global_load_dword v74, v15, s[10:11] offset:2368
	global_load_dword v75, v15, s[4:5] offset:2432
	global_load_dword v76, v15, s[10:11] offset:2432
	global_load_dword v77, v15, s[4:5] offset:2496
	global_load_dword v78, v15, s[10:11] offset:2496
	s_nop 0
	global_load_dwordx4 v[28:31], v[10:11], off offset:272
	global_load_dwordx4 v[32:35], v[10:11], off offset:256
	v_lshlrev_b64 v[16:17], 2, v[18:19]
	v_lshl_add_u64 v[38:39], s[4:5], 0, v[16:17]
	v_lshl_add_u64 v[16:17], s[10:11], 0, v[16:17]
	v_or_b32_e32 v18, 0x410, v14
	global_load_dword v79, v[16:17], off
	v_lshlrev_b64 v[16:17], 2, v[18:19]
	global_load_dword v15, v[38:39], off
	v_lshl_add_u64 v[38:39], s[4:5], 0, v[16:17]
	v_lshl_add_u64 v[16:17], s[10:11], 0, v[16:17]
	v_or_b32_e32 v18, 0x420, v14
	global_load_dword v81, v[16:17], off
	v_lshlrev_b64 v[16:17], 2, v[18:19]
	global_load_dword v80, v[38:39], off
	v_lshl_add_u64 v[38:39], s[4:5], 0, v[16:17]
	v_lshl_add_u64 v[16:17], s[10:11], 0, v[16:17]
	v_or_b32_e32 v18, 0x430, v14
	global_load_dword v83, v[16:17], off
	v_lshlrev_b64 v[16:17], 2, v[18:19]
	global_load_dword v82, v[38:39], off
	v_lshl_add_u64 v[38:39], s[4:5], 0, v[16:17]
	v_lshl_add_u64 v[16:17], s[10:11], 0, v[16:17]
	v_or_b32_e32 v18, 0x440, v14
	global_load_dword v85, v[16:17], off
	v_lshlrev_b64 v[16:17], 2, v[18:19]
	global_load_dword v84, v[38:39], off
	v_lshl_add_u64 v[38:39], s[4:5], 0, v[16:17]
	v_lshl_add_u64 v[16:17], s[10:11], 0, v[16:17]
	v_or_b32_e32 v18, 0x450, v14
	global_load_dword v87, v[16:17], off
	v_lshlrev_b64 v[16:17], 2, v[18:19]
	global_load_dword v86, v[38:39], off
	v_lshl_add_u64 v[38:39], s[4:5], 0, v[16:17]
	v_lshl_add_u64 v[16:17], s[10:11], 0, v[16:17]
	v_or_b32_e32 v18, 0x460, v14
	global_load_dword v89, v[16:17], off
	v_lshlrev_b64 v[16:17], 2, v[18:19]
	global_load_dword v88, v[38:39], off
	v_lshl_add_u64 v[38:39], s[4:5], 0, v[16:17]
	v_lshl_add_u64 v[16:17], s[10:11], 0, v[16:17]
	v_or_b32_e32 v18, 0x470, v14
	global_load_dword v91, v[16:17], off
	v_lshlrev_b64 v[16:17], 2, v[18:19]
	global_load_dword v90, v[38:39], off
	v_lshl_add_u64 v[38:39], s[4:5], 0, v[16:17]
	v_lshl_add_u64 v[16:17], s[10:11], 0, v[16:17]
	v_or_b32_e32 v18, 0x600, v14
	global_load_dword v92, v[38:39], off
	global_load_dword v93, v[16:17], off
	s_nop 0
	v_lshlrev_b64 v[16:17], 2, v[18:19]
	v_lshl_add_u64 v[46:47], s[4:5], 0, v[16:17]
	v_lshl_add_u64 v[16:17], s[10:11], 0, v[16:17]
	v_or_b32_e32 v18, 0x610, v14
	global_load_dword v95, v[16:17], off
	v_lshlrev_b64 v[16:17], 2, v[18:19]
	global_load_dword v94, v[46:47], off
	v_lshl_add_u64 v[46:47], s[4:5], 0, v[16:17]
	v_lshl_add_u64 v[16:17], s[10:11], 0, v[16:17]
	v_or_b32_e32 v18, 0x620, v14
	global_load_dword v97, v[16:17], off
	v_lshlrev_b64 v[16:17], 2, v[18:19]
	global_load_dword v96, v[46:47], off
	v_lshl_add_u64 v[46:47], s[4:5], 0, v[16:17]
	v_lshl_add_u64 v[16:17], s[10:11], 0, v[16:17]
	v_or_b32_e32 v18, 0x630, v14
	global_load_dword v99, v[16:17], off
	v_lshlrev_b64 v[16:17], 2, v[18:19]
	global_load_dword v98, v[46:47], off
	v_lshl_add_u64 v[46:47], s[4:5], 0, v[16:17]
	v_lshl_add_u64 v[16:17], s[10:11], 0, v[16:17]
	v_or_b32_e32 v18, 0x640, v14
	global_load_dword v101, v[16:17], off
	v_lshlrev_b64 v[16:17], 2, v[18:19]
	global_load_dword v100, v[46:47], off
	v_lshl_add_u64 v[46:47], s[4:5], 0, v[16:17]
	v_lshl_add_u64 v[16:17], s[10:11], 0, v[16:17]
	v_or_b32_e32 v18, 0x650, v14
	global_load_dword v103, v[16:17], off
	v_lshlrev_b64 v[16:17], 2, v[18:19]
	global_load_dword v102, v[46:47], off
	v_lshl_add_u64 v[46:47], s[4:5], 0, v[16:17]
	v_lshl_add_u64 v[16:17], s[10:11], 0, v[16:17]
	v_or_b32_e32 v18, 0x660, v14
	global_load_dword v105, v[16:17], off
	v_lshlrev_b64 v[16:17], 2, v[18:19]
	global_load_dword v104, v[46:47], off
	v_lshl_add_u64 v[46:47], s[4:5], 0, v[16:17]
	v_lshl_add_u64 v[16:17], s[10:11], 0, v[16:17]
	v_or_b32_e32 v18, 0x670, v14
	global_load_dword v107, v[16:17], off
	v_lshlrev_b64 v[16:17], 2, v[18:19]
	global_load_dword v106, v[46:47], off
	v_lshl_add_u64 v[46:47], s[4:5], 0, v[16:17]
	v_lshl_add_u64 v[16:17], s[10:11], 0, v[16:17]
	global_load_dword v18, v[46:47], off
	s_mov_b32 s23, 0
	global_load_dword v16, v[16:17], off
	s_load_dwordx2 s[24:25], s[0:1], 0x88
	s_load_dwordx4 s[12:15], s[0:1], 0x78
	s_load_dwordx4 s[16:19], s[0:1], 0x50
	s_waitcnt vmcnt(60)
	v_cvt_pk_f16_f32 v6, v6, v7
	v_cvt_pk_f16_f32 v7, v8, v9
	v_cvt_pk_f16_f32 v8, v2, v3
	v_cvt_pk_f16_f32 v9, v4, v5
	v_cvt_pk_f16_f32 v2, v37, v49
	v_cvt_pk_f16_f32 v3, v51, v53
	s_waitcnt vmcnt(57)
	v_cvt_pk_f16_f32 v4, v55, v57
	s_waitcnt vmcnt(53)
	v_cvt_pk_f16_f32 v5, v59, v61
	v_cvt_pk_f16_f32 v46, v48, v50
	v_cvt_pk_f16_f32 v47, v52, v54
	v_mfma_f32_16x16x32_f16 a[0:3], v[6:9], v[2:5], 0
	global_store_dwordx4 v108, v[6:9], s[26:27] offset:0
	v_cvt_pk_f16_f32 v48, v56, v58
	s_waitcnt vmcnt(53)
	v_cvt_pk_f16_f32 v49, v60, v62
	s_waitcnt vmcnt(51)
	v_cvt_pk_f16_f32 v2, v24, v25
	v_cvt_pk_f16_f32 v3, v26, v27
	v_cvt_pk_f16_f32 v4, v20, v21
	v_cvt_pk_f16_f32 v5, v22, v23
	v_mfma_f32_16x16x32_f16 a[4:7], v[6:9], v[46:49], 0
	s_waitcnt vmcnt(48)
	v_cvt_pk_f16_f32 v6, v63, v65
	s_waitcnt vmcnt(47)
	v_cvt_pk_f16_f32 v20, v64, v66
	s_waitcnt vmcnt(44)
	v_cvt_pk_f16_f32 v7, v67, v69
	s_waitcnt vmcnt(40)
	v_cvt_pk_f16_f32 v8, v71, v73
	s_waitcnt vmcnt(36)
	v_cvt_pk_f16_f32 v9, v75, v77
	v_cvt_pk_f16_f32 v21, v68, v70
	v_cvt_pk_f16_f32 v22, v72, v74
	s_waitcnt vmcnt(35)
	v_cvt_pk_f16_f32 v23, v76, v78
	v_mfma_f32_16x16x32_f16 a[0:3], v[2:5], v[6:9], a[0:3]
	global_store_dwordx4 v108, v[2:5], s[26:27] offset:64
	s_waitcnt vmcnt(30)
	v_cvt_pk_f16_f32 v6, v15, v80
	s_waitcnt vmcnt(26)
	v_cvt_pk_f16_f32 v7, v82, v84
	s_waitcnt vmcnt(22)
	v_cvt_pk_f16_f32 v8, v86, v88
	v_mfma_f32_16x16x32_f16 a[4:7], v[2:5], v[20:23], a[4:7]
	v_cvt_pk_f16_f32 v2, v32, v33
	v_cvt_pk_f16_f32 v3, v34, v35
	v_cvt_pk_f16_f32 v4, v28, v29
	v_cvt_pk_f16_f32 v5, v30, v31
	v_cvt_pk_f16_f32 v20, v79, v81
	s_waitcnt vmcnt(19)
	v_cvt_pk_f16_f32 v9, v90, v92
	v_cvt_pk_f16_f32 v21, v83, v85
	v_cvt_pk_f16_f32 v22, v87, v89
	s_waitcnt vmcnt(18)
	v_cvt_pk_f16_f32 v23, v91, v93
	v_mfma_f32_16x16x32_f16 a[0:3], v[2:5], v[6:9], a[0:3]
	global_store_dwordx4 v108, v[2:5], s[26:27] offset:128
	s_waitcnt vmcnt(15)
	v_cvt_pk_f16_f32 v6, v94, v96
	s_waitcnt vmcnt(11)
	v_cvt_pk_f16_f32 v7, v98, v100
	s_waitcnt vmcnt(7)
	v_cvt_pk_f16_f32 v8, v102, v104
	v_mfma_f32_16x16x32_f16 a[8:11], v[2:5], v[20:23], a[4:7]
	v_cvt_pk_f16_f32 v2, v144, v145
	v_cvt_pk_f16_f32 v3, v146, v147
	v_cvt_pk_f16_f32 v4, v148, v149
	v_cvt_pk_f16_f32 v5, v150, v151
	v_cvt_pk_f16_f32 v20, v95, v97
	s_waitcnt vmcnt(4)
	v_cvt_pk_f16_f32 v9, v106, v18
	v_cvt_pk_f16_f32 v21, v99, v101
	v_cvt_pk_f16_f32 v22, v103, v105
	s_waitcnt vmcnt(3)
	v_cvt_pk_f16_f32 v23, v107, v16
	v_mfma_f32_16x16x32_f16 a[4:7], v[2:5], v[6:9], a[0:3]
	global_store_dwordx4 v108, v[2:5], s[26:27] offset:192
	s_nop 0
	v_mfma_f32_16x16x32_f16 a[0:3], v[2:5], v[20:23], a[8:11]
	v_or_b32_e32 v18, 0x800, v14
	v_lshlrev_b64 v[16:17], 2, v[18:19]
	v_lshl_add_u64 v[20:21], s[4:5], 0, v[16:17]
	v_lshl_add_u64 v[16:17], s[10:11], 0, v[16:17]
	v_or_b32_e32 v18, 0x810, v14
	global_load_dword v46, v[16:17], off
	v_lshlrev_b64 v[16:17], 2, v[18:19]
	global_load_dword v37, v[20:21], off
	v_lshl_add_u64 v[20:21], s[4:5], 0, v[16:17]
	v_lshl_add_u64 v[16:17], s[10:11], 0, v[16:17]
	v_or_b32_e32 v18, 0x820, v14
	global_load_dword v48, v[16:17], off
	v_lshlrev_b64 v[16:17], 2, v[18:19]
	global_load_dword v47, v[20:21], off
	v_lshl_add_u64 v[20:21], s[4:5], 0, v[16:17]
	v_lshl_add_u64 v[16:17], s[10:11], 0, v[16:17]
	v_or_b32_e32 v18, 0x830, v14
	global_load_dword v50, v[16:17], off
	v_lshlrev_b64 v[16:17], 2, v[18:19]
	global_load_dword v49, v[20:21], off
	v_lshl_add_u64 v[20:21], s[4:5], 0, v[16:17]
	v_lshl_add_u64 v[16:17], s[10:11], 0, v[16:17]
	v_or_b32_e32 v18, 0x840, v14
	global_load_dword v52, v[16:17], off
	v_lshlrev_b64 v[16:17], 2, v[18:19]
	global_load_dword v51, v[20:21], off
	v_lshl_add_u64 v[20:21], s[4:5], 0, v[16:17]
	v_lshl_add_u64 v[16:17], s[10:11], 0, v[16:17]
	v_or_b32_e32 v18, 0x850, v14
	global_load_dword v54, v[16:17], off
	v_lshlrev_b64 v[16:17], 2, v[18:19]
	global_load_dword v53, v[20:21], off
	v_lshl_add_u64 v[20:21], s[4:5], 0, v[16:17]
	v_lshl_add_u64 v[16:17], s[10:11], 0, v[16:17]
	v_or_b32_e32 v18, 0x860, v14
	global_load_dword v56, v[16:17], off
	v_lshlrev_b64 v[16:17], 2, v[18:19]
	global_load_dword v55, v[20:21], off
	v_lshl_add_u64 v[20:21], s[4:5], 0, v[16:17]
	v_lshl_add_u64 v[16:17], s[10:11], 0, v[16:17]
	v_or_b32_e32 v18, 0x870, v14
	global_load_dword v58, v[16:17], off
	v_lshlrev_b64 v[16:17], 2, v[18:19]
	global_load_dword v57, v[20:21], off
	v_lshl_add_u64 v[20:21], s[4:5], 0, v[16:17]
	v_lshl_add_u64 v[16:17], s[10:11], 0, v[16:17]
	v_or_b32_e32 v18, 0xa00, v14
	global_load_dword v59, v[20:21], off
	global_load_dword v60, v[16:17], off
	s_nop 0
	v_lshlrev_b64 v[16:17], 2, v[18:19]
	v_lshl_add_u64 v[28:29], s[4:5], 0, v[16:17]
	v_lshl_add_u64 v[16:17], s[10:11], 0, v[16:17]
	v_or_b32_e32 v18, 0xa10, v14
	global_load_dword v62, v[16:17], off
	v_lshlrev_b64 v[16:17], 2, v[18:19]
	global_load_dword v61, v[28:29], off
	v_lshl_add_u64 v[28:29], s[4:5], 0, v[16:17]
	v_lshl_add_u64 v[16:17], s[10:11], 0, v[16:17]
	v_or_b32_e32 v18, 0xa20, v14
	global_load_dword v64, v[16:17], off
	v_lshlrev_b64 v[16:17], 2, v[18:19]
	global_load_dword v63, v[28:29], off
	v_lshl_add_u64 v[28:29], s[4:5], 0, v[16:17]
	v_lshl_add_u64 v[16:17], s[10:11], 0, v[16:17]
	v_or_b32_e32 v18, 0xa30, v14
	global_load_dword v66, v[16:17], off
	v_lshlrev_b64 v[16:17], 2, v[18:19]
	global_load_dword v65, v[28:29], off
	v_lshl_add_u64 v[28:29], s[4:5], 0, v[16:17]
	v_lshl_add_u64 v[16:17], s[10:11], 0, v[16:17]
	v_or_b32_e32 v18, 0xa40, v14
	global_load_dword v68, v[16:17], off
	v_lshlrev_b64 v[16:17], 2, v[18:19]
	global_load_dword v67, v[28:29], off
	v_lshl_add_u64 v[28:29], s[4:5], 0, v[16:17]
	v_lshl_add_u64 v[16:17], s[10:11], 0, v[16:17]
	v_or_b32_e32 v18, 0xa50, v14
	global_load_dword v70, v[16:17], off
	v_lshlrev_b64 v[16:17], 2, v[18:19]
	global_load_dword v69, v[28:29], off
	v_lshl_add_u64 v[28:29], s[4:5], 0, v[16:17]
	v_lshl_add_u64 v[16:17], s[10:11], 0, v[16:17]
	v_or_b32_e32 v18, 0xa60, v14
	global_load_dword v72, v[16:17], off
	v_lshlrev_b64 v[16:17], 2, v[18:19]
	global_load_dword v71, v[28:29], off
	v_lshl_add_u64 v[28:29], s[4:5], 0, v[16:17]
	v_lshl_add_u64 v[16:17], s[10:11], 0, v[16:17]
	v_or_b32_e32 v18, 0xa70, v14
	global_load_dword v74, v[16:17], off
	v_lshlrev_b64 v[16:17], 2, v[18:19]
	global_load_dword v73, v[28:29], off
	v_lshl_add_u64 v[28:29], s[4:5], 0, v[16:17]
	v_lshl_add_u64 v[16:17], s[10:11], 0, v[16:17]
	v_or_b32_e32 v18, 0xc00, v14
	global_load_dword v75, v[28:29], off
	global_load_dword v76, v[16:17], off
	s_nop 0
	v_lshlrev_b64 v[16:17], 2, v[18:19]
	v_lshl_add_u64 v[38:39], s[4:5], 0, v[16:17]
	v_lshl_add_u64 v[16:17], s[10:11], 0, v[16:17]
	v_or_b32_e32 v18, 0xc10, v14
	global_load_dword v78, v[16:17], off
	v_lshlrev_b64 v[16:17], 2, v[18:19]
	global_load_dword v77, v[38:39], off
	v_lshl_add_u64 v[38:39], s[4:5], 0, v[16:17]
	v_lshl_add_u64 v[16:17], s[10:11], 0, v[16:17]
	v_or_b32_e32 v18, 0xc20, v14
	global_load_dword v80, v[16:17], off
	v_lshlrev_b64 v[16:17], 2, v[18:19]
	global_load_dword v79, v[38:39], off
	v_lshl_add_u64 v[38:39], s[4:5], 0, v[16:17]
	v_lshl_add_u64 v[16:17], s[10:11], 0, v[16:17]
	v_or_b32_e32 v18, 0xc30, v14
	global_load_dword v82, v[16:17], off
	v_lshlrev_b64 v[16:17], 2, v[18:19]
	global_load_dword v81, v[38:39], off
	v_lshl_add_u64 v[38:39], s[4:5], 0, v[16:17]
	v_lshl_add_u64 v[16:17], s[10:11], 0, v[16:17]
	v_or_b32_e32 v18, 0xc40, v14
	global_load_dword v84, v[16:17], off
	v_lshlrev_b64 v[16:17], 2, v[18:19]
	global_load_dword v83, v[38:39], off
	v_lshl_add_u64 v[38:39], s[4:5], 0, v[16:17]
	v_lshl_add_u64 v[16:17], s[10:11], 0, v[16:17]
	v_or_b32_e32 v18, 0xc50, v14
	global_load_dword v86, v[16:17], off
	v_lshlrev_b64 v[16:17], 2, v[18:19]
	global_load_dword v85, v[38:39], off
	v_lshl_add_u64 v[38:39], s[4:5], 0, v[16:17]
	v_lshl_add_u64 v[16:17], s[10:11], 0, v[16:17]
	v_or_b32_e32 v18, 0xc60, v14
	global_load_dword v88, v[16:17], off
	v_lshlrev_b64 v[16:17], 2, v[18:19]
	global_load_dword v87, v[38:39], off
	v_lshl_add_u64 v[38:39], s[4:5], 0, v[16:17]
	v_lshl_add_u64 v[16:17], s[10:11], 0, v[16:17]
	v_or_b32_e32 v18, 0xc70, v14
	global_load_dword v90, v[16:17], off
	v_lshlrev_b64 v[16:17], 2, v[18:19]
	global_load_dword v89, v[38:39], off
	v_lshl_add_u64 v[38:39], s[4:5], 0, v[16:17]
	v_lshl_add_u64 v[16:17], s[10:11], 0, v[16:17]
	v_or_b32_e32 v18, 0xe00, v14
	global_load_dword v91, v[38:39], off
	global_load_dword v92, v[16:17], off
	s_nop 0
	v_lshlrev_b64 v[10:11], 2, v[18:19]
	v_lshl_add_u64 v[16:17], s[4:5], 0, v[10:11]
	v_lshl_add_u64 v[10:11], s[10:11], 0, v[10:11]
	v_or_b32_e32 v18, 0xe10, v14
	global_load_dword v94, v[10:11], off
	v_lshlrev_b64 v[10:11], 2, v[18:19]
	global_load_dword v93, v[16:17], off
	v_lshl_add_u64 v[16:17], s[4:5], 0, v[10:11]
	v_lshl_add_u64 v[10:11], s[10:11], 0, v[10:11]
	v_or_b32_e32 v18, 0xe20, v14
	global_load_dword v96, v[10:11], off
	v_lshlrev_b64 v[10:11], 2, v[18:19]
	global_load_dword v95, v[16:17], off
	v_lshl_add_u64 v[16:17], s[4:5], 0, v[10:11]
	v_lshl_add_u64 v[10:11], s[10:11], 0, v[10:11]
	v_or_b32_e32 v18, 0xe30, v14
	global_load_dword v98, v[10:11], off
	v_lshlrev_b64 v[10:11], 2, v[18:19]
	global_load_dword v97, v[16:17], off
	v_lshl_add_u64 v[16:17], s[4:5], 0, v[10:11]
	v_lshl_add_u64 v[10:11], s[10:11], 0, v[10:11]
	v_or_b32_e32 v18, 0xe40, v14
	global_load_dword v100, v[10:11], off
	v_lshlrev_b64 v[10:11], 2, v[18:19]
	global_load_dword v99, v[16:17], off
	v_lshl_add_u64 v[16:17], s[4:5], 0, v[10:11]
	v_lshl_add_u64 v[10:11], s[10:11], 0, v[10:11]
	v_or_b32_e32 v18, 0xe50, v14
	global_load_dword v102, v[10:11], off
	v_lshlrev_b64 v[10:11], 2, v[18:19]
	global_load_dword v101, v[16:17], off
	v_lshl_add_u64 v[16:17], s[4:5], 0, v[10:11]
	v_lshl_add_u64 v[10:11], s[10:11], 0, v[10:11]
	v_or_b32_e32 v18, 0xe60, v14
	global_load_dword v104, v[10:11], off
	v_lshlrev_b64 v[10:11], 2, v[18:19]
	global_load_dword v103, v[16:17], off
	v_lshl_add_u64 v[16:17], s[4:5], 0, v[10:11]
	v_lshl_add_u64 v[10:11], s[10:11], 0, v[10:11]
	v_or_b32_e32 v18, 0xe70, v14
	global_load_dword v106, v[10:11], off
	v_lshlrev_b64 v[10:11], 2, v[18:19]
	v_lshl_add_u64 v[14:15], s[4:5], 0, v[10:11]
	v_lshl_add_u64 v[10:11], s[10:11], 0, v[10:11]
	global_load_dword v105, v[16:17], off
	global_load_dword v18, v[14:15], off
	s_nop 0
	global_load_dword v10, v[10:11], off
	s_waitcnt vmcnt(56)
	v_cvt_pk_f16_f32 v6, v112, v113
	v_cvt_pk_f16_f32 v7, v114, v115
	v_cvt_pk_f16_f32 v8, v116, v117
	v_cvt_pk_f16_f32 v9, v118, v119
	v_cvt_pk_f16_f32 v2, v37, v47
	v_cvt_pk_f16_f32 v3, v49, v51
	s_waitcnt vmcnt(52)
	v_cvt_pk_f16_f32 v4, v53, v55
	s_waitcnt vmcnt(49)
	v_cvt_pk_f16_f32 v5, v57, v59
	s_waitcnt vmcnt(45)
	v_cvt_pk_f16_f32 v14, v62, v64
	s_waitcnt vmcnt(41)
	v_cvt_pk_f16_f32 v15, v66, v68
	v_mfma_f32_16x16x32_f16 a[4:7], v[6:9], v[2:5], a[4:7]
	global_store_dwordx4 v108, v[6:9], s[26:27] offset:256
	v_cvt_pk_f16_f32 v2, v46, v48
	v_cvt_pk_f16_f32 v3, v50, v52
	v_cvt_pk_f16_f32 v4, v54, v56
	v_cvt_pk_f16_f32 v5, v58, v60
	s_waitcnt vmcnt(38)
	v_cvt_pk_f16_f32 v16, v70, v72
	s_waitcnt vmcnt(33)
	v_cvt_pk_f16_f32 v17, v74, v76
	v_mfma_f32_16x16x32_f16 a[0:3], v[6:9], v[2:5], a[0:3]
	v_cvt_pk_f16_f32 v2, v120, v121
	v_cvt_pk_f16_f32 v3, v122, v123
	v_cvt_pk_f16_f32 v4, v124, v125
	v_cvt_pk_f16_f32 v5, v126, v127
	v_cvt_pk_f16_f32 v6, v61, v63
	v_cvt_pk_f16_f32 v7, v65, v67
	v_cvt_pk_f16_f32 v8, v69, v71
	v_cvt_pk_f16_f32 v9, v73, v75
	v_mfma_f32_16x16x32_f16 a[0:3], v[2:5], v[14:17], a[0:3]
	global_store_dwordx4 v108, v[2:5], s[26:27] offset:320
	s_waitcnt vmcnt(31)
	v_cvt_pk_f16_f32 v14, v78, v80
	s_waitcnt vmcnt(27)
	v_cvt_pk_f16_f32 v15, v82, v84
	s_waitcnt vmcnt(23)
	v_cvt_pk_f16_f32 v16, v86, v88
	v_mfma_f32_16x16x32_f16 a[4:7], v[2:5], v[6:9], a[4:7]
	v_cvt_pk_f16_f32 v2, v128, v129
	v_cvt_pk_f16_f32 v3, v130, v131
	v_cvt_pk_f16_f32 v4, v132, v133
	v_cvt_pk_f16_f32 v5, v134, v135
	v_cvt_pk_f16_f32 v6, v77, v79
	v_cvt_pk_f16_f32 v7, v81, v83
	s_waitcnt vmcnt(22)
	v_cvt_pk_f16_f32 v8, v85, v87
	s_waitcnt vmcnt(19)
	v_cvt_pk_f16_f32 v9, v89, v91
	s_waitcnt vmcnt(18)
	v_cvt_pk_f16_f32 v17, v90, v92
	v_mfma_f32_16x16x32_f16 a[4:7], v[2:5], v[6:9], a[4:7]
	global_store_dwordx4 v108, v[2:5], s[26:27] offset:384
	s_waitcnt vmcnt(15)
	v_cvt_pk_f16_f32 v6, v93, v95
	s_waitcnt vmcnt(11)
	v_cvt_pk_f16_f32 v7, v97, v99
	s_waitcnt vmcnt(7)
	v_cvt_pk_f16_f32 v8, v101, v103
	v_mfma_f32_16x16x32_f16 a[0:3], v[2:5], v[14:17], a[0:3]
	v_cvt_pk_f16_f32 v2, v136, v137
	v_cvt_pk_f16_f32 v3, v138, v139
	v_cvt_pk_f16_f32 v4, v140, v141
	v_cvt_pk_f16_f32 v5, v142, v143
	v_cvt_pk_f16_f32 v14, v94, v96
	s_waitcnt vmcnt(4)
	v_cvt_pk_f16_f32 v9, v105, v18
	v_cvt_pk_f16_f32 v15, v98, v100
	v_cvt_pk_f16_f32 v16, v102, v104
	s_waitcnt vmcnt(3)
	v_cvt_pk_f16_f32 v17, v106, v10
	v_mfma_f32_16x16x32_f16 a[4:7], v[2:5], v[6:9], a[4:7]
	global_store_dwordx4 v108, v[2:5], s[26:27] offset:448
	s_nop 0
	v_mfma_f32_16x16x32_f16 a[0:3], v[2:5], v[14:17], a[0:3]
	v_lshlrev_b32_e32 v2, 11, v1
	v_lshlrev_b32_e32 v3, 2, v12
	v_lshlrev_b32_e32 v4, 8, v13
	v_lshlrev_b32_e32 v18, 2, v0
	s_movk_i32 s4, 0x3c0
	v_or3_b32 v2, v2, v3, v4
	v_and_or_b32 v10, v18, s4, v3
	ds_write_b32 v2, a4
	ds_write_b32 v2, a0 offset:1024
	ds_write_b32 v2, a5 offset:64
	ds_write_b32 v2, a1 offset:1088
	ds_write_b32 v2, a6 offset:128
	ds_write_b32 v2, a2 offset:1152
	ds_write_b32 v2, a7 offset:192
	ds_write_b32 v2, a3 offset:1216
	s_waitcnt lgkmcnt(0)
	s_barrier
	ds_read2st64_b32 v[2:3], v10 offset1:4
	ds_read2st64_b32 v[4:5], v10 offset0:8 offset1:12
	ds_read2st64_b32 v[6:7], v10 offset0:16 offset1:20
	ds_read2st64_b32 v[8:9], v10 offset0:24 offset1:28
	s_movk_i32 s4, 0x1000
	v_or_b32_e32 v20, 0x2000, v18
	s_waitcnt lgkmcnt(2)
	v_add_f32_e32 v2, v2, v4
	v_add_f32_e32 v3, v3, v5
	s_waitcnt lgkmcnt(1)
	v_add_f32_e32 v2, v2, v6
	v_add_f32_e32 v3, v3, v7
	v_lshl_add_u64 v[6:7], s[6:7], 0, v[18:19]
	s_waitcnt lgkmcnt(0)
	v_add_f32_e32 v2, v2, v8
	v_add_f32_e32 v3, v3, v9
	v_add_co_u32_e32 v4, vcc, s4, v6
	ds_write2st64_b32 v10, v2, v3 offset0:32 offset1:36
	v_or_b32_e32 v10, 0x1000, v18
	v_addc_co_u32_e32 v5, vcc, 0, v7, vcc
	s_waitcnt lgkmcnt(0)
	s_barrier
	global_load_dword v2, v18, s[6:7] offset:2048
	global_load_dword v3, v18, s[6:7] offset:3072
	global_load_dword v57, v10, s[6:7]
	global_load_dword v49, v[4:5], off offset:1024
	global_load_dword v50, v[4:5], off offset:2048
	global_load_dword v44, v[4:5], off offset:3072
	global_load_dword v51, v10, s[16:17]
	global_load_dword v13, v18, s[6:7]
	s_nop 0
	global_load_dword v5, v18, s[16:17]
	global_load_dword v10, v18, s[6:7] offset:1024
	global_load_dword v11, v18, s[16:17] offset:1024
	global_load_dword v4, v18, s[16:17] offset:2048
	global_load_dword v42, v18, s[8:9]
	global_load_dword v12, v18, s[16:17] offset:3072
	global_load_dword v40, v18, s[18:19]
	v_lshl_add_u64 v[8:9], s[16:17], 0, v[18:19]
	v_add_co_u32_e32 v14, vcc, s4, v8
	s_movk_i32 s4, 0x2000
	s_nop 0
	v_addc_co_u32_e32 v15, vcc, 0, v9, vcc
	v_add_co_u32_e32 v16, vcc, s4, v6
	s_mov_b32 s5, 0xc2000000
	s_nop 0
	v_addc_co_u32_e32 v17, vcc, 0, v7, vcc
	global_load_dword v56, v[14:15], off offset:1024
	global_load_dword v54, v[14:15], off offset:2048
	global_load_dword v52, v[14:15], off offset:3072
	global_load_dword v53, v20, s[6:7]
	global_load_dword v43, v[16:17], off offset:1024
	global_load_dword v30, v[16:17], off offset:2048
	global_load_dword v31, v[16:17], off offset:3072
	global_load_dword v45, v20, s[16:17]
	v_add_co_u32_e32 v14, vcc, s4, v8
	s_movk_i32 s4, 0x3000
	s_nop 0
	v_addc_co_u32_e32 v15, vcc, 0, v9, vcc
	v_add_co_u32_e32 v6, vcc, s4, v6
	v_or_b32_e32 v16, 0x3000, v18
	s_nop 0
	v_addc_co_u32_e32 v7, vcc, 0, v7, vcc
	global_load_dword v46, v[14:15], off offset:1024
	global_load_dword v34, v[14:15], off offset:2048
	global_load_dword v35, v[14:15], off offset:3072
	global_load_dword v32, v16, s[6:7]
	global_load_dword v33, v[6:7], off offset:1024
	global_load_dword v20, v[6:7], off offset:2048
	global_load_dword v21, v[6:7], off offset:3072
	global_load_dword v22, v16, s[16:17]
	v_add_co_u32_e32 v6, vcc, s4, v8
	s_and_b32 s4, s2, 0xffffff80
	s_nop 0
	v_addc_co_u32_e32 v7, vcc, 0, v9, vcc
	global_load_dword v23, v[6:7], off offset:1024
	global_load_dword v24, v[6:7], off offset:2048
	global_load_dword v25, v[6:7], off offset:3072
	v_lshl_or_b32 v6, v1, 5, s4
	s_lshr_b32 s4, s2, 2
	v_and_or_b32 v70, s4, 31, v6
	ds_read_b128 v[6:9], v19 offset:8192
	ds_read_b128 v[14:17], v19 offset:9216
	ds_read_b128 v[26:29], v19 offset:8208
	ds_read_b128 v[58:61], v19 offset:8224
	ds_read_b128 v[62:65], v19 offset:8240
	v_lshlrev_b32_e32 v18, 1, v36
	ds_read_b128 v[66:69], v19 offset:9232
	v_lshl_add_u64 v[72:73], s[24:25], 0, v[18:19]
	v_mov_b32_e32 v38, 0x42000000
	v_ashrrev_i32_e32 v71, 31, v70
	s_and_b32 s4, s22, 48
	s_lshl_b32 s22, s4, 7
	s_lshl_b32 s4, s4, 1
	s_waitcnt vmcnt(21) lgkmcnt(5)
	v_fma_f32 v18, v13, v6, v42
	v_fmac_f32_e32 v18, v10, v7
	s_waitcnt vmcnt(19) lgkmcnt(4)
	v_fma_f32 v37, v5, v14, v40
	v_fmac_f32_e32 v37, v11, v15
	v_fmac_f32_e32 v18, v2, v8
	v_fmac_f32_e32 v37, v4, v16
	v_fmac_f32_e32 v18, v3, v9
	v_fmac_f32_e32 v37, v12, v17
	ds_read_b128 v[6:9], v19 offset:9248
	s_waitcnt lgkmcnt(4)
	v_fmac_f32_e32 v18, v57, v26
	s_waitcnt lgkmcnt(1)
	v_fmac_f32_e32 v37, v51, v66
	v_fmac_f32_e32 v18, v49, v27
	s_waitcnt vmcnt(18)
	v_fmac_f32_e32 v37, v56, v67
	v_fmac_f32_e32 v18, v50, v28
	s_waitcnt vmcnt(17)
	v_fmac_f32_e32 v37, v54, v68
	v_fmac_f32_e32 v18, v44, v29
	s_waitcnt vmcnt(16)
	v_fmac_f32_e32 v37, v52, v69
	s_waitcnt vmcnt(15)
	v_fmac_f32_e32 v18, v53, v58
	s_waitcnt vmcnt(11) lgkmcnt(0)
	v_fmac_f32_e32 v37, v45, v6
	v_fmac_f32_e32 v18, v43, v59
	s_waitcnt vmcnt(10)
	v_fmac_f32_e32 v37, v46, v7
	v_pk_mul_f32 v[6:7], v[30:31], v[60:61]
	ds_read_b128 v[14:17], v19 offset:9264
	v_add_f32_e32 v6, v18, v6
	v_add_f32_e32 v18, v6, v7
	s_waitcnt vmcnt(8)
	v_pk_mul_f32 v[6:7], v[34:35], v[8:9]
	v_lshlrev_b64 v[26:27], 13, v[70:71]
	v_add_f32_e32 v6, v37, v6
	v_add_f32_e32 v8, v6, v7
	s_waitcnt vmcnt(6)
	v_pk_mul_f32 v[6:7], v[32:33], v[62:63]
	s_nop 0
	v_add_f32_e32 v6, v18, v6
	v_add_f32_e32 v9, v6, v7
	s_waitcnt vmcnt(2) lgkmcnt(0)
	v_pk_mul_f32 v[6:7], v[22:23], v[14:15]
	s_nop 0
	v_add_f32_e32 v6, v8, v6
	v_add_f32_e32 v8, v6, v7
	v_pk_mul_f32 v[6:7], v[20:21], v[64:65]
	s_nop 0
	v_add_f32_e32 v6, v9, v6
	v_add_f32_e32 v9, v6, v7
	s_waitcnt vmcnt(0)
	v_pk_mul_f32 v[6:7], v[24:25], v[16:17]
	s_nop 0
	v_add_f32_e32 v6, v8, v6
	v_add_f32_e32 v6, v6, v7
	v_med3_f32 v6, v6, s5, v38
	v_mul_f32_e32 v6, 0x3fb8aa3b, v6
	v_exp_f32_e32 v18, v6
	v_med3_f32 v6, v9, s5, v38
	v_mul_f32_e32 v6, 0x3fb8aa3b, v6
	v_exp_f32_e32 v37, v6
	v_lshl_add_u64 v[6:7], v[72:73], 0, v[26:27]
	v_cvt_pk_bf16_f32 v8, v18, s0
	v_lshl_add_u64 v[28:29], v[6:7], 0, s[22:23]
	global_store_short v[28:29], v8, off
	ds_read_b128 v[6:9], v19 offset:8256
	ds_read_b128 v[14:17], v19 offset:9280
	ds_read_b128 v[58:61], v19 offset:8272
	ds_read_b128 v[62:65], v19 offset:8288
	ds_read_b128 v[66:69], v19 offset:8304
	ds_read_b128 v[70:73], v19 offset:9296
	s_waitcnt lgkmcnt(5)
	v_fma_f32 v39, v13, v6, v42
	s_waitcnt lgkmcnt(4)
	v_fma_f32 v41, v5, v14, v40
	v_fmac_f32_e32 v39, v10, v7
	v_fmac_f32_e32 v41, v11, v15
	v_fmac_f32_e32 v39, v2, v8
	v_fmac_f32_e32 v41, v4, v16
	v_fmac_f32_e32 v39, v3, v9
	v_fmac_f32_e32 v41, v12, v17
	ds_read_b128 v[6:9], v19 offset:9312
	s_waitcnt lgkmcnt(4)
	v_fmac_f32_e32 v39, v57, v58
	s_waitcnt lgkmcnt(1)
	v_fmac_f32_e32 v41, v51, v70
	v_fmac_f32_e32 v39, v49, v59
	v_fmac_f32_e32 v41, v56, v71
	v_fmac_f32_e32 v39, v50, v60
	v_fmac_f32_e32 v41, v54, v72
	v_fmac_f32_e32 v39, v44, v61
	v_fmac_f32_e32 v41, v52, v73
	v_fmac_f32_e32 v39, v53, v62
	s_waitcnt lgkmcnt(0)
	v_fmac_f32_e32 v41, v45, v6
	v_fmac_f32_e32 v39, v43, v63
	v_fmac_f32_e32 v41, v46, v7
	v_pk_mul_f32 v[6:7], v[30:31], v[64:65]
	ds_read_b128 v[14:17], v19 offset:9328
	v_add_f32_e32 v6, v39, v6
	v_add_f32_e32 v39, v6, v7
	v_pk_mul_f32 v[6:7], v[34:35], v[8:9]
	s_nop 0
	v_add_f32_e32 v6, v41, v6
	v_add_f32_e32 v8, v6, v7
	v_pk_mul_f32 v[6:7], v[32:33], v[66:67]
	s_nop 0
	v_add_f32_e32 v6, v39, v6
	v_add_f32_e32 v9, v6, v7
	s_waitcnt lgkmcnt(0)
	v_pk_mul_f32 v[6:7], v[22:23], v[14:15]
	s_nop 0
	v_add_f32_e32 v6, v8, v6
	v_add_f32_e32 v8, v6, v7
	v_pk_mul_f32 v[6:7], v[20:21], v[68:69]
	s_nop 0
	v_add_f32_e32 v6, v9, v6
	v_add_f32_e32 v9, v6, v7
	v_pk_mul_f32 v[6:7], v[24:25], v[16:17]
	s_nop 0
	v_add_f32_e32 v6, v8, v6
	v_add_f32_e32 v6, v6, v7
	v_med3_f32 v6, v6, s5, v38
	v_mul_f32_e32 v6, 0x3fb8aa3b, v6
	v_med3_f32 v7, v9, s5, v38
	v_exp_f32_e32 v39, v6
	v_mul_f32_e32 v41, 0x3fb8aa3b, v7
	ds_read_b128 v[6:9], v19 offset:8320
	ds_read_b128 v[14:17], v19 offset:9344
	ds_read_b128 v[58:61], v19 offset:8336
	ds_read_b128 v[62:65], v19 offset:9360
	v_cvt_pk_bf16_f32 v47, v39, s0
	global_store_short v[28:29], v47, off offset:128
	s_waitcnt lgkmcnt(3)
	v_fma_f32 v47, v13, v6, v42
	s_waitcnt lgkmcnt(2)
	v_fma_f32 v48, v5, v14, v40
	v_fmac_f32_e32 v47, v10, v7
	v_fmac_f32_e32 v48, v11, v15
	v_fmac_f32_e32 v47, v2, v8
	v_fmac_f32_e32 v48, v4, v16
	v_fmac_f32_e32 v47, v3, v9
	v_fmac_f32_e32 v48, v12, v17
	s_waitcnt lgkmcnt(1)
	v_fmac_f32_e32 v47, v57, v58
	ds_read_b128 v[6:9], v19 offset:8352
	ds_read_b128 v[14:17], v19 offset:9376
	v_fmac_f32_e32 v47, v49, v59
	s_waitcnt lgkmcnt(2)
	v_fmac_f32_e32 v48, v51, v62
	v_fmac_f32_e32 v47, v50, v60
	v_fmac_f32_e32 v48, v56, v63
	v_fmac_f32_e32 v47, v44, v61
	v_fmac_f32_e32 v48, v54, v64
	ds_read_b128 v[58:61], v19 offset:8368
	s_waitcnt lgkmcnt(2)
	v_fmac_f32_e32 v47, v53, v6
	v_fmac_f32_e32 v48, v52, v65
	v_fmac_f32_e32 v47, v43, v7
	v_pk_mul_f32 v[6:7], v[30:31], v[8:9]
	ds_read_b128 v[62:65], v19 offset:9392
	s_waitcnt lgkmcnt(2)
	v_fmac_f32_e32 v48, v45, v14
	v_add_f32_e32 v6, v47, v6
	v_fmac_f32_e32 v48, v46, v15
	v_add_f32_e32 v8, v6, v7
	v_pk_mul_f32 v[6:7], v[34:35], v[16:17]
	v_exp_f32_e32 v41, v41
	v_add_f32_e32 v6, v48, v6
	v_add_f32_e32 v9, v6, v7
	s_waitcnt lgkmcnt(1)
	v_pk_mul_f32 v[6:7], v[32:33], v[58:59]
	s_nop 0
	v_add_f32_e32 v6, v8, v6
	v_add_f32_e32 v8, v6, v7
	s_waitcnt lgkmcnt(0)
	v_pk_mul_f32 v[6:7], v[22:23], v[62:63]
	s_nop 0
	v_add_f32_e32 v6, v9, v6
	v_add_f32_e32 v9, v6, v7
	v_pk_mul_f32 v[6:7], v[20:21], v[60:61]
	s_nop 0
	v_add_f32_e32 v6, v8, v6
	v_add_f32_e32 v8, v6, v7
	v_pk_mul_f32 v[6:7], v[24:25], v[64:65]
	s_nop 0
	v_add_f32_e32 v6, v9, v6
	v_add_f32_e32 v6, v6, v7
	v_med3_f32 v6, v6, s5, v38
	v_mul_f32_e32 v6, 0x3fb8aa3b, v6
	v_exp_f32_e32 v47, v6
	v_med3_f32 v6, v8, s5, v38
	v_mul_f32_e32 v6, 0x3fb8aa3b, v6
	v_exp_f32_e32 v48, v6
	v_cvt_pk_bf16_f32 v6, v47, s0
	global_store_short v[28:29], v6, off offset:256
	ds_read_b128 v[6:9], v19 offset:8384
	ds_read_b128 v[14:17], v19 offset:9408
	ds_read_b128 v[58:61], v19 offset:8400
	ds_read_b128 v[62:65], v19 offset:8416
	ds_read_b128 v[66:69], v19 offset:8432
	ds_read_b128 v[70:73], v19 offset:9424
	s_waitcnt lgkmcnt(5)
	v_fma_f32 v55, v13, v6, v42
	s_waitcnt lgkmcnt(4)
	v_fma_f32 v74, v5, v14, v40
	v_fmac_f32_e32 v55, v10, v7
	v_fmac_f32_e32 v74, v11, v15
	v_fmac_f32_e32 v55, v2, v8
	v_fmac_f32_e32 v74, v4, v16
	v_fmac_f32_e32 v55, v3, v9
	v_fmac_f32_e32 v74, v12, v17
	ds_read_b128 v[6:9], v19 offset:9440
	s_waitcnt lgkmcnt(4)
	v_fmac_f32_e32 v55, v57, v58
	s_waitcnt lgkmcnt(1)
	v_fmac_f32_e32 v74, v51, v70
	v_fmac_f32_e32 v55, v49, v59
	v_fmac_f32_e32 v74, v56, v71
	v_fmac_f32_e32 v55, v50, v60
	v_fmac_f32_e32 v74, v54, v72
	v_fmac_f32_e32 v55, v44, v61
	v_fmac_f32_e32 v74, v52, v73
	v_fmac_f32_e32 v55, v53, v62
	s_waitcnt lgkmcnt(0)
	v_fmac_f32_e32 v74, v45, v6
	v_fmac_f32_e32 v55, v43, v63
	v_fmac_f32_e32 v74, v46, v7
	v_pk_mul_f32 v[6:7], v[30:31], v[64:65]
	ds_read_b128 v[14:17], v19 offset:9456
	v_add_f32_e32 v6, v55, v6
	v_add_f32_e32 v55, v6, v7
	v_pk_mul_f32 v[6:7], v[34:35], v[8:9]
	s_nop 0
	v_add_f32_e32 v6, v74, v6
	v_add_f32_e32 v8, v6, v7
	v_pk_mul_f32 v[6:7], v[32:33], v[66:67]
	s_nop 0
	v_add_f32_e32 v6, v55, v6
	v_add_f32_e32 v9, v6, v7
	s_waitcnt lgkmcnt(0)
	v_pk_mul_f32 v[6:7], v[22:23], v[14:15]
	s_nop 0
	v_add_f32_e32 v6, v8, v6
	v_add_f32_e32 v8, v6, v7
	v_pk_mul_f32 v[6:7], v[20:21], v[68:69]
	s_nop 0
	v_add_f32_e32 v6, v9, v6
	v_add_f32_e32 v9, v6, v7
	v_pk_mul_f32 v[6:7], v[24:25], v[16:17]
	s_nop 0
	v_add_f32_e32 v6, v8, v6
	v_add_f32_e32 v6, v6, v7
	v_med3_f32 v6, v6, s5, v38
	v_mul_f32_e32 v6, 0x3fb8aa3b, v6
	v_med3_f32 v7, v9, s5, v38
	v_exp_f32_e32 v55, v6
	v_mul_f32_e32 v58, 0x3fb8aa3b, v7
	ds_read_b128 v[6:9], v19 offset:8448
	ds_read_b128 v[14:17], v19 offset:9472
	ds_read_b128 v[60:63], v19 offset:8464
	ds_read_b128 v[64:67], v19 offset:9488
	v_cvt_pk_bf16_f32 v59, v55, s0
	global_store_short v[28:29], v59, off offset:384
	s_waitcnt lgkmcnt(3)
	v_fma_f32 v59, v13, v6, v42
	s_waitcnt lgkmcnt(2)
	v_fma_f32 v68, v5, v14, v40
	v_fmac_f32_e32 v59, v10, v7
	v_fmac_f32_e32 v68, v11, v15
	v_fmac_f32_e32 v59, v2, v8
	v_fmac_f32_e32 v68, v4, v16
	v_fmac_f32_e32 v59, v3, v9
	v_fmac_f32_e32 v68, v12, v17
	s_waitcnt lgkmcnt(1)
	v_fmac_f32_e32 v59, v57, v60
	ds_read_b128 v[6:9], v19 offset:8480
	ds_read_b128 v[14:17], v19 offset:9504
	v_fmac_f32_e32 v59, v49, v61
	s_waitcnt lgkmcnt(2)
	v_fmac_f32_e32 v68, v51, v64
	v_fmac_f32_e32 v59, v50, v62
	v_fmac_f32_e32 v68, v56, v65
	v_fmac_f32_e32 v59, v44, v63
	v_fmac_f32_e32 v68, v54, v66
	ds_read_b128 v[60:63], v19 offset:8496
	s_waitcnt lgkmcnt(2)
	v_fmac_f32_e32 v59, v53, v6
	v_fmac_f32_e32 v68, v52, v67
	v_fmac_f32_e32 v59, v43, v7
	v_pk_mul_f32 v[6:7], v[30:31], v[8:9]
	ds_read_b128 v[64:67], v19 offset:9520
	s_waitcnt lgkmcnt(2)
	v_fmac_f32_e32 v68, v45, v14
	v_add_f32_e32 v6, v59, v6
	v_fmac_f32_e32 v68, v46, v15
	v_add_f32_e32 v8, v6, v7
	v_pk_mul_f32 v[6:7], v[34:35], v[16:17]
	v_exp_f32_e32 v58, v58
	v_add_f32_e32 v6, v68, v6
	v_add_f32_e32 v9, v6, v7
	s_waitcnt lgkmcnt(1)
	v_pk_mul_f32 v[6:7], v[32:33], v[60:61]
	s_nop 0
	v_add_f32_e32 v6, v8, v6
	v_add_f32_e32 v8, v6, v7
	s_waitcnt lgkmcnt(0)
	v_pk_mul_f32 v[6:7], v[22:23], v[64:65]
	s_nop 0
	v_add_f32_e32 v6, v9, v6
	v_add_f32_e32 v9, v6, v7
	v_pk_mul_f32 v[6:7], v[20:21], v[62:63]
	s_nop 0
	v_add_f32_e32 v6, v8, v6
	v_add_f32_e32 v8, v6, v7
	v_pk_mul_f32 v[6:7], v[24:25], v[66:67]
	s_nop 0
	v_add_f32_e32 v6, v9, v6
	v_add_f32_e32 v6, v6, v7
	v_med3_f32 v6, v6, s5, v38
	v_mul_f32_e32 v6, 0x3fb8aa3b, v6
	v_exp_f32_e32 v59, v6
	v_med3_f32 v6, v8, s5, v38
	v_mul_f32_e32 v6, 0x3fb8aa3b, v6
	v_exp_f32_e32 v60, v6
	v_cvt_pk_bf16_f32 v6, v59, s0
	global_store_short v[28:29], v6, off offset:512
	ds_read_b128 v[6:9], v19 offset:8512
	ds_read_b128 v[14:17], v19 offset:9536
	ds_read_b128 v[62:65], v19 offset:8528
	ds_read_b128 v[66:69], v19 offset:8544
	ds_read_b128 v[70:73], v19 offset:8560
	ds_read_b128 v[74:77], v19 offset:9552
	s_waitcnt lgkmcnt(5)
	v_fma_f32 v61, v13, v6, v42
	s_waitcnt lgkmcnt(4)
	v_fma_f32 v78, v5, v14, v40
	v_fmac_f32_e32 v61, v10, v7
	v_fmac_f32_e32 v78, v11, v15
	v_fmac_f32_e32 v61, v2, v8
	v_fmac_f32_e32 v78, v4, v16
	v_fmac_f32_e32 v61, v3, v9
	v_fmac_f32_e32 v78, v12, v17
	ds_read_b128 v[6:9], v19 offset:9568
	s_waitcnt lgkmcnt(4)
	v_fmac_f32_e32 v61, v57, v62
	s_waitcnt lgkmcnt(1)
	v_fmac_f32_e32 v78, v51, v74
	v_fmac_f32_e32 v61, v49, v63
	v_fmac_f32_e32 v78, v56, v75
	v_fmac_f32_e32 v61, v50, v64
	v_fmac_f32_e32 v78, v54, v76
	v_fmac_f32_e32 v61, v44, v65
	v_fmac_f32_e32 v78, v52, v77
	v_fmac_f32_e32 v61, v53, v66
	s_waitcnt lgkmcnt(0)
	v_fmac_f32_e32 v78, v45, v6
	v_fmac_f32_e32 v61, v43, v67
	v_fmac_f32_e32 v78, v46, v7
	v_pk_mul_f32 v[6:7], v[30:31], v[68:69]
	ds_read_b128 v[14:17], v19 offset:9584
	v_add_f32_e32 v6, v61, v6
	v_add_f32_e32 v61, v6, v7
	v_pk_mul_f32 v[6:7], v[34:35], v[8:9]
	s_nop 0
	v_add_f32_e32 v6, v78, v6
	v_add_f32_e32 v8, v6, v7
	v_pk_mul_f32 v[6:7], v[32:33], v[70:71]
	s_nop 0
	v_add_f32_e32 v6, v61, v6
	v_add_f32_e32 v9, v6, v7
	s_waitcnt lgkmcnt(0)
	v_pk_mul_f32 v[6:7], v[22:23], v[14:15]
	s_nop 0
	v_add_f32_e32 v6, v8, v6
	v_add_f32_e32 v8, v6, v7
	v_pk_mul_f32 v[6:7], v[20:21], v[72:73]
	s_nop 0
	v_add_f32_e32 v6, v9, v6
	v_add_f32_e32 v9, v6, v7
	v_pk_mul_f32 v[6:7], v[24:25], v[16:17]
	s_nop 0
	v_add_f32_e32 v6, v8, v6
	v_add_f32_e32 v6, v6, v7
	v_med3_f32 v6, v6, s5, v38
	v_mul_f32_e32 v6, 0x3fb8aa3b, v6
	v_med3_f32 v7, v9, s5, v38
	v_exp_f32_e32 v61, v6
	v_mul_f32_e32 v62, 0x3fb8aa3b, v7
	ds_read_b128 v[6:9], v19 offset:8576
	ds_read_b128 v[14:17], v19 offset:9600
	ds_read_b128 v[64:67], v19 offset:8592
	ds_read_b128 v[68:71], v19 offset:9616
	v_cvt_pk_bf16_f32 v63, v61, s0
	global_store_short v[28:29], v63, off offset:640
	s_waitcnt lgkmcnt(3)
	v_fma_f32 v63, v13, v6, v42
	s_waitcnt lgkmcnt(2)
	v_fma_f32 v72, v5, v14, v40
	v_fmac_f32_e32 v63, v10, v7
	v_fmac_f32_e32 v72, v11, v15
	v_fmac_f32_e32 v63, v2, v8
	v_fmac_f32_e32 v72, v4, v16
	v_fmac_f32_e32 v63, v3, v9
	v_fmac_f32_e32 v72, v12, v17
	s_waitcnt lgkmcnt(1)
	v_fmac_f32_e32 v63, v57, v64
	ds_read_b128 v[6:9], v19 offset:8608
	ds_read_b128 v[14:17], v19 offset:9632
	v_fmac_f32_e32 v63, v49, v65
	s_waitcnt lgkmcnt(2)
	v_fmac_f32_e32 v72, v51, v68
	v_fmac_f32_e32 v63, v50, v66
	v_fmac_f32_e32 v72, v56, v69
	v_fmac_f32_e32 v63, v44, v67
	v_fmac_f32_e32 v72, v54, v70
	ds_read_b128 v[64:67], v19 offset:8624
	s_waitcnt lgkmcnt(2)
	v_fmac_f32_e32 v63, v53, v6
	v_fmac_f32_e32 v72, v52, v71
	v_fmac_f32_e32 v63, v43, v7
	v_pk_mul_f32 v[6:7], v[30:31], v[8:9]
	ds_read_b128 v[68:71], v19 offset:9648
	s_waitcnt lgkmcnt(2)
	v_fmac_f32_e32 v72, v45, v14
	v_add_f32_e32 v6, v63, v6
	v_fmac_f32_e32 v72, v46, v15
	v_add_f32_e32 v8, v6, v7
	v_pk_mul_f32 v[6:7], v[34:35], v[16:17]
	v_exp_f32_e32 v62, v62
	v_add_f32_e32 v6, v72, v6
	v_add_f32_e32 v9, v6, v7
	s_waitcnt lgkmcnt(1)
	v_pk_mul_f32 v[6:7], v[32:33], v[64:65]
	s_nop 0
	v_add_f32_e32 v6, v8, v6
	v_add_f32_e32 v8, v6, v7
	s_waitcnt lgkmcnt(0)
	v_pk_mul_f32 v[6:7], v[22:23], v[68:69]
	s_nop 0
	v_add_f32_e32 v6, v9, v6
	v_add_f32_e32 v9, v6, v7
	v_pk_mul_f32 v[6:7], v[20:21], v[66:67]
	s_nop 0
	v_add_f32_e32 v6, v8, v6
	v_add_f32_e32 v8, v6, v7
	v_pk_mul_f32 v[6:7], v[24:25], v[70:71]
	s_nop 0
	v_add_f32_e32 v6, v9, v6
	v_add_f32_e32 v6, v6, v7
	v_med3_f32 v6, v6, s5, v38
	v_mul_f32_e32 v6, 0x3fb8aa3b, v6
	v_exp_f32_e32 v63, v6
	v_med3_f32 v6, v8, s5, v38
	v_mul_f32_e32 v6, 0x3fb8aa3b, v6
	v_exp_f32_e32 v64, v6
	v_cvt_pk_bf16_f32 v6, v63, s0
	global_store_short v[28:29], v6, off offset:768
	ds_read_b128 v[6:9], v19 offset:8640
	ds_read_b128 v[14:17], v19 offset:9664
	ds_read_b128 v[66:69], v19 offset:8656
	ds_read_b128 v[70:73], v19 offset:8672
	ds_read_b128 v[74:77], v19 offset:8688
	ds_read_b128 v[78:81], v19 offset:9680
	s_waitcnt lgkmcnt(5)
	v_fma_f32 v65, v13, v6, v42
	s_waitcnt lgkmcnt(4)
	v_fma_f32 v82, v5, v14, v40
	v_fmac_f32_e32 v65, v10, v7
	v_fmac_f32_e32 v82, v11, v15
	v_fmac_f32_e32 v65, v2, v8
	v_fmac_f32_e32 v82, v4, v16
	v_fmac_f32_e32 v65, v3, v9
	v_fmac_f32_e32 v82, v12, v17
	ds_read_b128 v[6:9], v19 offset:9696
	s_waitcnt lgkmcnt(4)
	v_fmac_f32_e32 v65, v57, v66
	s_waitcnt lgkmcnt(1)
	v_fmac_f32_e32 v82, v51, v78
	v_fmac_f32_e32 v65, v49, v67
	v_fmac_f32_e32 v82, v56, v79
	v_fmac_f32_e32 v65, v50, v68
	v_fmac_f32_e32 v82, v54, v80
	v_fmac_f32_e32 v65, v44, v69
	v_fmac_f32_e32 v82, v52, v81
	v_fmac_f32_e32 v65, v53, v70
	s_waitcnt lgkmcnt(0)
	v_fmac_f32_e32 v82, v45, v6
	v_fmac_f32_e32 v65, v43, v71
	v_fmac_f32_e32 v82, v46, v7
	v_pk_mul_f32 v[6:7], v[30:31], v[72:73]
	ds_read_b128 v[14:17], v19 offset:9712
	v_add_f32_e32 v6, v65, v6
	v_add_f32_e32 v65, v6, v7
	v_pk_mul_f32 v[6:7], v[34:35], v[8:9]
	s_nop 0
	v_add_f32_e32 v6, v82, v6
	v_add_f32_e32 v8, v6, v7
	v_pk_mul_f32 v[6:7], v[32:33], v[74:75]
	s_nop 0
	v_add_f32_e32 v6, v65, v6
	v_add_f32_e32 v9, v6, v7
	s_waitcnt lgkmcnt(0)
	v_pk_mul_f32 v[6:7], v[22:23], v[14:15]
	s_nop 0
	v_add_f32_e32 v6, v8, v6
	v_add_f32_e32 v8, v6, v7
	v_pk_mul_f32 v[6:7], v[20:21], v[76:77]
	s_nop 0
	v_add_f32_e32 v6, v9, v6
	v_add_f32_e32 v9, v6, v7
	v_pk_mul_f32 v[6:7], v[24:25], v[16:17]
	s_nop 0
	v_add_f32_e32 v6, v8, v6
	v_add_f32_e32 v6, v6, v7
	v_med3_f32 v6, v6, s5, v38
	v_mul_f32_e32 v6, 0x3fb8aa3b, v6
	v_exp_f32_e32 v65, v6
	v_med3_f32 v6, v9, s5, v38
	v_mul_f32_e32 v6, 0x3fb8aa3b, v6
	v_exp_f32_e32 v66, v6
	v_cvt_pk_bf16_f32 v6, v65, s0
	global_store_short v[28:29], v6, off offset:896
	ds_read_b128 v[6:9], v19 offset:8704
	ds_read_b128 v[14:17], v19 offset:9728
	ds_read_b128 v[68:71], v19 offset:8720
	ds_read_b128 v[72:75], v19 offset:8736
	ds_read_b128 v[76:79], v19 offset:8752
	ds_read_b128 v[80:83], v19 offset:9744
	s_waitcnt lgkmcnt(5)
	v_fma_f32 v67, v13, v6, v42
	s_waitcnt lgkmcnt(4)
	v_fma_f32 v84, v5, v14, v40
	v_fmac_f32_e32 v67, v10, v7
	v_fmac_f32_e32 v84, v11, v15
	v_fmac_f32_e32 v67, v2, v8
	v_fmac_f32_e32 v84, v4, v16
	v_fmac_f32_e32 v67, v3, v9
	v_fmac_f32_e32 v84, v12, v17
	ds_read_b128 v[6:9], v19 offset:9760
	s_waitcnt lgkmcnt(4)
	v_fmac_f32_e32 v67, v57, v68
	s_waitcnt lgkmcnt(1)
	v_fmac_f32_e32 v84, v51, v80
	v_fmac_f32_e32 v67, v49, v69
	v_fmac_f32_e32 v84, v56, v81
	v_fmac_f32_e32 v67, v50, v70
	v_fmac_f32_e32 v84, v54, v82
	v_fmac_f32_e32 v67, v44, v71
	v_fmac_f32_e32 v84, v52, v83
	v_fmac_f32_e32 v67, v53, v72
	s_waitcnt lgkmcnt(0)
	v_fmac_f32_e32 v84, v45, v6
	v_fmac_f32_e32 v67, v43, v73
	v_fmac_f32_e32 v84, v46, v7
	v_pk_mul_f32 v[6:7], v[30:31], v[74:75]
	ds_read_b128 v[14:17], v19 offset:9776
	v_add_f32_e32 v6, v67, v6
	v_add_f32_e32 v67, v6, v7
	v_pk_mul_f32 v[6:7], v[34:35], v[8:9]
	s_nop 0
	v_add_f32_e32 v6, v84, v6
	v_add_f32_e32 v8, v6, v7
	v_pk_mul_f32 v[6:7], v[32:33], v[76:77]
	s_nop 0
	v_add_f32_e32 v6, v67, v6
	v_add_f32_e32 v9, v6, v7
	s_waitcnt lgkmcnt(0)
	v_pk_mul_f32 v[6:7], v[22:23], v[14:15]
	s_nop 0
	v_add_f32_e32 v6, v8, v6
	v_add_f32_e32 v8, v6, v7
	v_pk_mul_f32 v[6:7], v[20:21], v[78:79]
	s_nop 0
	v_add_f32_e32 v6, v9, v6
	v_add_f32_e32 v9, v6, v7
	v_pk_mul_f32 v[6:7], v[24:25], v[16:17]
	s_nop 0
	v_add_f32_e32 v6, v8, v6
	v_add_f32_e32 v6, v6, v7
	v_med3_f32 v6, v6, s5, v38
	v_mul_f32_e32 v6, 0x3fb8aa3b, v6
	v_exp_f32_e32 v67, v6
	v_med3_f32 v6, v9, s5, v38
	v_mul_f32_e32 v6, 0x3fb8aa3b, v6
	v_exp_f32_e32 v68, v6
	v_cvt_pk_bf16_f32 v6, v67, s0
	global_store_short v[28:29], v6, off offset:1024
	ds_read_b128 v[6:9], v19 offset:8768
	ds_read_b128 v[14:17], v19 offset:9792
	ds_read_b128 v[70:73], v19 offset:8784
	ds_read_b128 v[74:77], v19 offset:8800
	ds_read_b128 v[78:81], v19 offset:8816
	ds_read_b128 v[82:85], v19 offset:9808
	s_waitcnt lgkmcnt(5)
	v_fma_f32 v69, v13, v6, v42
	s_waitcnt lgkmcnt(4)
	v_fma_f32 v86, v5, v14, v40
	v_fmac_f32_e32 v69, v10, v7
	v_fmac_f32_e32 v86, v11, v15
	v_fmac_f32_e32 v69, v2, v8
	v_fmac_f32_e32 v86, v4, v16
	v_fmac_f32_e32 v69, v3, v9
	v_fmac_f32_e32 v86, v12, v17
	ds_read_b128 v[6:9], v19 offset:9824
	s_waitcnt lgkmcnt(4)
	v_fmac_f32_e32 v69, v57, v70
	s_waitcnt lgkmcnt(1)
	v_fmac_f32_e32 v86, v51, v82
	v_fmac_f32_e32 v69, v49, v71
	v_fmac_f32_e32 v86, v56, v83
	v_fmac_f32_e32 v69, v50, v72
	v_fmac_f32_e32 v86, v54, v84
	v_fmac_f32_e32 v69, v44, v73
	v_fmac_f32_e32 v86, v52, v85
	v_fmac_f32_e32 v69, v53, v74
	s_waitcnt lgkmcnt(0)
	v_fmac_f32_e32 v86, v45, v6
	v_fmac_f32_e32 v69, v43, v75
	v_fmac_f32_e32 v86, v46, v7
	v_pk_mul_f32 v[6:7], v[30:31], v[76:77]
	ds_read_b128 v[14:17], v19 offset:9840
	v_add_f32_e32 v6, v69, v6
	v_add_f32_e32 v69, v6, v7
	v_pk_mul_f32 v[6:7], v[34:35], v[8:9]
	ds_read_b128 v[72:75], v19 offset:8848
	v_add_f32_e32 v6, v86, v6
	v_add_f32_e32 v8, v6, v7
	v_pk_mul_f32 v[6:7], v[32:33], v[78:79]
	ds_read_b128 v[76:79], v19 offset:9872
	v_add_f32_e32 v6, v69, v6
	v_add_f32_e32 v9, v6, v7
	s_waitcnt lgkmcnt(2)
	v_pk_mul_f32 v[6:7], v[22:23], v[14:15]
	s_nop 0
	v_add_f32_e32 v6, v8, v6
	v_add_f32_e32 v8, v6, v7
	v_pk_mul_f32 v[6:7], v[20:21], v[80:81]
	s_nop 0
	v_add_f32_e32 v6, v9, v6
	v_add_f32_e32 v9, v6, v7
	v_pk_mul_f32 v[6:7], v[24:25], v[16:17]
	ds_read_b128 v[14:17], v19 offset:9856
	v_add_f32_e32 v6, v8, v6
	v_add_f32_e32 v6, v6, v7
	v_med3_f32 v6, v6, s5, v38
	v_mul_f32_e32 v6, 0x3fb8aa3b, v6
	v_exp_f32_e32 v69, v6
	v_med3_f32 v6, v9, s5, v38
	v_mul_f32_e32 v6, 0x3fb8aa3b, v6
	v_exp_f32_e32 v70, v6
	ds_read_b128 v[6:9], v19 offset:8832
	v_cvt_pk_bf16_f32 v71, v69, s0
	global_store_short v[28:29], v71, off offset:1152
	s_waitcnt lgkmcnt(1)
	v_fma_f32 v80, v5, v14, v40
	v_fmac_f32_e32 v80, v11, v15
	s_waitcnt lgkmcnt(0)
	v_fma_f32 v71, v13, v6, v42
	v_fmac_f32_e32 v71, v10, v7
	v_fmac_f32_e32 v71, v2, v8
	v_fmac_f32_e32 v71, v3, v9
	v_fmac_f32_e32 v71, v57, v72
	v_fmac_f32_e32 v80, v4, v16
	v_fmac_f32_e32 v71, v49, v73
	v_fmac_f32_e32 v80, v12, v17
	ds_read_b128 v[6:9], v19 offset:8864
	ds_read_b128 v[14:17], v19 offset:8880
	v_fmac_f32_e32 v71, v50, v74
	v_fmac_f32_e32 v71, v44, v75
	ds_read_b128 v[72:75], v19 offset:9888
	v_fmac_f32_e32 v80, v51, v76
	v_fmac_f32_e32 v80, v56, v77
	v_fmac_f32_e32 v80, v54, v78
	s_waitcnt lgkmcnt(2)
	v_fmac_f32_e32 v71, v53, v6
	v_fmac_f32_e32 v80, v52, v79
	v_fmac_f32_e32 v71, v43, v7
	v_pk_mul_f32 v[6:7], v[30:31], v[8:9]
	ds_read_b128 v[76:79], v19 offset:9904
	s_waitcnt lgkmcnt(1)
	v_fmac_f32_e32 v80, v45, v72
	v_add_f32_e32 v6, v71, v6
	v_fmac_f32_e32 v80, v46, v73
	v_add_f32_e32 v8, v6, v7
	v_pk_mul_f32 v[6:7], v[34:35], v[74:75]
	s_nop 0
	v_add_f32_e32 v6, v80, v6
	v_add_f32_e32 v9, v6, v7
	v_pk_mul_f32 v[6:7], v[32:33], v[14:15]
	s_nop 0
	v_add_f32_e32 v6, v8, v6
	v_add_f32_e32 v8, v6, v7
	s_waitcnt lgkmcnt(0)
	v_pk_mul_f32 v[6:7], v[22:23], v[76:77]
	ds_read_b128 v[74:77], v19 offset:8912
	v_add_f32_e32 v6, v9, v6
	v_add_f32_e32 v9, v6, v7
	v_pk_mul_f32 v[6:7], v[20:21], v[16:17]
	ds_read_b128 v[14:17], v19 offset:9920
	v_add_f32_e32 v6, v8, v6
	v_add_f32_e32 v8, v6, v7
	v_pk_mul_f32 v[6:7], v[24:25], v[78:79]
	ds_read_b128 v[78:81], v19 offset:9936
	v_add_f32_e32 v6, v9, v6
	v_add_f32_e32 v6, v6, v7
	v_med3_f32 v6, v6, s5, v38
	v_mul_f32_e32 v6, 0x3fb8aa3b, v6
	v_exp_f32_e32 v71, v6
	v_med3_f32 v6, v8, s5, v38
	v_mul_f32_e32 v6, 0x3fb8aa3b, v6
	v_exp_f32_e32 v72, v6
	ds_read_b128 v[6:9], v19 offset:8896
	v_cvt_pk_bf16_f32 v73, v71, s0
	global_store_short v[28:29], v73, off offset:1280
	s_waitcnt lgkmcnt(2)
	v_fma_f32 v82, v5, v14, v40
	v_fmac_f32_e32 v82, v11, v15
	s_waitcnt lgkmcnt(0)
	v_fma_f32 v73, v13, v6, v42
	v_fmac_f32_e32 v73, v10, v7
	v_fmac_f32_e32 v73, v2, v8
	v_fmac_f32_e32 v73, v3, v9
	v_fmac_f32_e32 v73, v57, v74
	v_fmac_f32_e32 v82, v4, v16
	v_fmac_f32_e32 v73, v49, v75
	v_fmac_f32_e32 v82, v12, v17
	ds_read_b128 v[6:9], v19 offset:8928
	ds_read_b128 v[14:17], v19 offset:8944
	v_fmac_f32_e32 v73, v50, v76
	v_fmac_f32_e32 v73, v44, v77
	ds_read_b128 v[74:77], v19 offset:9952
	v_fmac_f32_e32 v82, v51, v78
	v_fmac_f32_e32 v82, v56, v79
	v_fmac_f32_e32 v82, v54, v80
	s_waitcnt lgkmcnt(2)
	v_fmac_f32_e32 v73, v53, v6
	v_fmac_f32_e32 v82, v52, v81
	v_fmac_f32_e32 v73, v43, v7
	v_pk_mul_f32 v[6:7], v[30:31], v[8:9]
	ds_read_b128 v[78:81], v19 offset:9968
	s_waitcnt lgkmcnt(1)
	v_fmac_f32_e32 v82, v45, v74
	v_add_f32_e32 v6, v73, v6
	v_fmac_f32_e32 v82, v46, v75
	v_add_f32_e32 v8, v6, v7
	v_pk_mul_f32 v[6:7], v[34:35], v[76:77]
	s_nop 0
	v_add_f32_e32 v6, v82, v6
	v_add_f32_e32 v9, v6, v7
	v_pk_mul_f32 v[6:7], v[32:33], v[14:15]
	s_nop 0
	v_add_f32_e32 v6, v8, v6
	v_add_f32_e32 v8, v6, v7
	s_waitcnt lgkmcnt(0)
	v_pk_mul_f32 v[6:7], v[22:23], v[78:79]
	s_nop 0
	v_add_f32_e32 v6, v9, v6
	v_add_f32_e32 v9, v6, v7
	v_pk_mul_f32 v[6:7], v[20:21], v[16:17]
	s_nop 0
	v_add_f32_e32 v6, v8, v6
	v_add_f32_e32 v8, v6, v7
	v_pk_mul_f32 v[6:7], v[24:25], v[80:81]
	s_nop 0
	v_add_f32_e32 v6, v9, v6
	v_add_f32_e32 v6, v6, v7
	v_med3_f32 v6, v6, s5, v38
	v_med3_f32 v7, v8, s5, v38
	v_mul_f32_e32 v6, 0x3fb8aa3b, v6
	v_mul_f32_e32 v7, 0x3fb8aa3b, v7
	v_exp_f32_e32 v73, v6
	v_exp_f32_e32 v74, v7
	ds_read_b128 v[6:9], v19 offset:8960
	ds_read_b128 v[14:17], v19 offset:9984
	ds_read_b128 v[76:79], v19 offset:8976
	v_cvt_pk_bf16_f32 v75, v73, s0
	global_store_short v[28:29], v75, off offset:1408
	s_waitcnt lgkmcnt(2)
	v_fma_f32 v75, v13, v6, v42
	v_fmac_f32_e32 v75, v10, v7
	ds_read_b128 v[80:83], v19 offset:10000
	v_fmac_f32_e32 v75, v2, v8
	s_waitcnt lgkmcnt(2)
	v_fma_f32 v84, v5, v14, v40
	v_fmac_f32_e32 v75, v3, v9
	v_fmac_f32_e32 v84, v11, v15
	ds_read_b128 v[6:9], v19 offset:8992
	s_waitcnt lgkmcnt(2)
	v_fmac_f32_e32 v75, v57, v76
	v_fmac_f32_e32 v84, v4, v16
	v_fmac_f32_e32 v75, v49, v77
	v_fmac_f32_e32 v84, v12, v17
	v_fmac_f32_e32 v75, v50, v78
	ds_read_b128 v[14:17], v19 offset:10016
	v_fmac_f32_e32 v75, v44, v79
	ds_read_b128 v[76:79], v19 offset:9008
	s_waitcnt lgkmcnt(3)
	v_fmac_f32_e32 v84, v51, v80
	v_fmac_f32_e32 v84, v56, v81
	v_fmac_f32_e32 v84, v54, v82
	s_waitcnt lgkmcnt(2)
	v_fmac_f32_e32 v75, v53, v6
	v_fmac_f32_e32 v84, v52, v83
	v_fmac_f32_e32 v75, v43, v7
	v_pk_mul_f32 v[6:7], v[30:31], v[8:9]
	ds_read_b128 v[80:83], v19 offset:10032
	s_waitcnt lgkmcnt(2)
	v_fmac_f32_e32 v84, v45, v14
	v_add_f32_e32 v6, v75, v6
	v_fmac_f32_e32 v84, v46, v15
	v_add_f32_e32 v8, v6, v7
	v_pk_mul_f32 v[6:7], v[34:35], v[16:17]
	s_nop 0
	v_add_f32_e32 v6, v84, v6
	v_add_f32_e32 v9, v6, v7
	s_waitcnt lgkmcnt(1)
	v_pk_mul_f32 v[6:7], v[32:33], v[76:77]
	s_nop 0
	v_add_f32_e32 v6, v8, v6
	v_add_f32_e32 v8, v6, v7
	s_waitcnt lgkmcnt(0)
	v_pk_mul_f32 v[6:7], v[22:23], v[80:81]
	s_nop 0
	v_add_f32_e32 v6, v9, v6
	v_add_f32_e32 v9, v6, v7
	v_pk_mul_f32 v[6:7], v[20:21], v[78:79]
	s_nop 0
	v_add_f32_e32 v6, v8, v6
	v_add_f32_e32 v8, v6, v7
	v_pk_mul_f32 v[6:7], v[24:25], v[82:83]
	s_nop 0
	v_add_f32_e32 v6, v9, v6
	v_add_f32_e32 v6, v6, v7
	v_med3_f32 v6, v6, s5, v38
	v_med3_f32 v7, v8, s5, v38
	v_mul_f32_e32 v6, 0x3fb8aa3b, v6
	v_mul_f32_e32 v7, 0x3fb8aa3b, v7
	v_exp_f32_e32 v75, v6
	v_exp_f32_e32 v76, v7
	ds_read_b128 v[6:9], v19 offset:9024
	ds_read_b128 v[14:17], v19 offset:10048
	ds_read_b128 v[78:81], v19 offset:9040
	v_cvt_pk_bf16_f32 v77, v75, s0
	global_store_short v[28:29], v77, off offset:1536
	s_waitcnt lgkmcnt(2)
	v_fma_f32 v77, v13, v6, v42
	v_fmac_f32_e32 v77, v10, v7
	ds_read_b128 v[82:85], v19 offset:10064
	v_fmac_f32_e32 v77, v2, v8
	s_waitcnt lgkmcnt(2)
	v_fma_f32 v86, v5, v14, v40
	v_fmac_f32_e32 v77, v3, v9
	v_fmac_f32_e32 v86, v11, v15
	ds_read_b128 v[6:9], v19 offset:9056
	s_waitcnt lgkmcnt(2)
	v_fmac_f32_e32 v77, v57, v78
	v_fmac_f32_e32 v86, v4, v16
	v_fmac_f32_e32 v77, v49, v79
	v_fmac_f32_e32 v86, v12, v17
	v_fmac_f32_e32 v77, v50, v80
	ds_read_b128 v[14:17], v19 offset:10080
	v_fmac_f32_e32 v77, v44, v81
	ds_read_b128 v[78:81], v19 offset:9072
	s_waitcnt lgkmcnt(3)
	v_fmac_f32_e32 v86, v51, v82
	v_fmac_f32_e32 v86, v56, v83
	v_fmac_f32_e32 v86, v54, v84
	s_waitcnt lgkmcnt(2)
	v_fmac_f32_e32 v77, v53, v6
	v_fmac_f32_e32 v86, v52, v85
	v_fmac_f32_e32 v77, v43, v7
	v_pk_mul_f32 v[6:7], v[30:31], v[8:9]
	ds_read_b128 v[82:85], v19 offset:10096
	s_waitcnt lgkmcnt(2)
	v_fmac_f32_e32 v86, v45, v14
	v_add_f32_e32 v6, v77, v6
	v_fmac_f32_e32 v86, v46, v15
	v_add_f32_e32 v8, v6, v7
	v_pk_mul_f32 v[6:7], v[34:35], v[16:17]
	s_nop 0
	v_add_f32_e32 v6, v86, v6
	v_add_f32_e32 v9, v6, v7
	s_waitcnt lgkmcnt(1)
	v_pk_mul_f32 v[6:7], v[32:33], v[78:79]
	s_nop 0
	v_add_f32_e32 v6, v8, v6
	v_add_f32_e32 v8, v6, v7
	s_waitcnt lgkmcnt(0)
	v_pk_mul_f32 v[6:7], v[22:23], v[82:83]
	s_nop 0
	v_add_f32_e32 v6, v9, v6
	v_add_f32_e32 v9, v6, v7
	v_pk_mul_f32 v[6:7], v[20:21], v[80:81]
	s_nop 0
	v_add_f32_e32 v6, v8, v6
	v_add_f32_e32 v8, v6, v7
	v_pk_mul_f32 v[6:7], v[24:25], v[84:85]
	s_nop 0
	v_add_f32_e32 v6, v9, v6
	v_add_f32_e32 v6, v6, v7
	v_med3_f32 v6, v6, s5, v38
	v_mul_f32_e32 v6, 0x3fb8aa3b, v6
	v_med3_f32 v7, v8, s5, v38
	v_exp_f32_e32 v77, v6
	v_mul_f32_e32 v6, 0x3fb8aa3b, v7
	v_exp_f32_e32 v78, v6
	ds_read_b128 v[6:9], v19 offset:9088
	v_cvt_pk_bf16_f32 v14, v77, s0
	global_store_short v[28:29], v14, off offset:1664
	ds_read_b128 v[14:17], v19 offset:9104
	ds_read_b128 v[80:83], v19 offset:10112
	s_waitcnt lgkmcnt(2)
	v_fma_f32 v79, v13, v6, v42
	v_fmac_f32_e32 v79, v10, v7
	v_fmac_f32_e32 v79, v2, v8
	v_fmac_f32_e32 v79, v3, v9
	ds_read_b128 v[6:9], v19 offset:10128
	s_waitcnt lgkmcnt(1)
	v_fma_f32 v86, v5, v80, v40
	v_fmac_f32_e32 v86, v11, v81
	v_fmac_f32_e32 v79, v57, v14
	v_fmac_f32_e32 v86, v4, v82
	v_fmac_f32_e32 v79, v49, v15
	v_fmac_f32_e32 v86, v12, v83
	v_fmac_f32_e32 v79, v50, v16
	v_fmac_f32_e32 v79, v44, v17
	ds_read_b128 v[14:17], v19 offset:9120
	s_waitcnt lgkmcnt(1)
	v_fmac_f32_e32 v86, v51, v6
	v_fmac_f32_e32 v86, v56, v7
	v_fmac_f32_e32 v86, v54, v8
	v_fmac_f32_e32 v86, v52, v9
	ds_read_b128 v[6:9], v19 offset:10144
	ds_read_b128 v[80:83], v19 offset:9136
	s_waitcnt lgkmcnt(2)
	v_fmac_f32_e32 v79, v53, v14
	v_fmac_f32_e32 v79, v43, v15
	v_pk_mul_f32 v[84:85], v[30:31], v[16:17]
	ds_read_b128 v[14:17], v19 offset:10160
	s_waitcnt lgkmcnt(2)
	v_fmac_f32_e32 v86, v45, v6
	v_add_f32_e32 v6, v79, v84
	v_fmac_f32_e32 v86, v46, v7
	v_add_f32_e32 v79, v6, v85
	v_pk_mul_f32 v[6:7], v[34:35], v[8:9]
	s_nop 0
	v_add_f32_e32 v6, v86, v6
	v_add_f32_e32 v8, v6, v7
	s_waitcnt lgkmcnt(1)
	v_pk_mul_f32 v[6:7], v[32:33], v[80:81]
	ds_read_b128 v[86:89], v19 offset:10176
	v_add_f32_e32 v6, v79, v6
	v_add_f32_e32 v9, v6, v7
	s_waitcnt lgkmcnt(1)
	v_pk_mul_f32 v[6:7], v[22:23], v[14:15]
	s_waitcnt lgkmcnt(0)
	v_fmac_f32_e32 v40, v5, v86
	v_add_f32_e32 v6, v8, v6
	v_add_f32_e32 v8, v6, v7
	v_pk_mul_f32 v[6:7], v[20:21], v[82:83]
	ds_read_b128 v[82:85], v19 offset:9152
	v_add_f32_e32 v6, v9, v6
	v_add_f32_e32 v9, v6, v7
	v_pk_mul_f32 v[6:7], v[24:25], v[16:17]
	ds_read_b128 v[14:17], v19 offset:10192
	v_add_f32_e32 v6, v8, v6
	v_add_f32_e32 v6, v6, v7
	v_med3_f32 v6, v6, s5, v38
	v_mul_f32_e32 v6, 0x3fb8aa3b, v6
	v_exp_f32_e32 v79, v6
	v_med3_f32 v7, v9, s5, v38
	v_mul_f32_e32 v7, 0x3fb8aa3b, v7
	v_exp_f32_e32 v80, v7
	v_cvt_pk_bf16_f32 v6, v79, s0
	global_store_short v[28:29], v6, off offset:1792
	ds_read_b128 v[6:9], v19 offset:9168
	s_waitcnt lgkmcnt(2)
	v_fmac_f32_e32 v42, v13, v82
	v_fmac_f32_e32 v42, v10, v83
	v_fmac_f32_e32 v40, v11, v87
	v_fmac_f32_e32 v42, v2, v84
	v_fmac_f32_e32 v42, v3, v85
	v_fmac_f32_e32 v40, v4, v88
	v_fmac_f32_e32 v40, v12, v89
	ds_read_b128 v[10:13], v19 offset:9184
	ds_read_b128 v[2:5], v19 offset:9200
	s_waitcnt lgkmcnt(2)
	v_fmac_f32_e32 v42, v57, v6
	v_fmac_f32_e32 v42, v49, v7
	ds_read_b128 v[82:85], v19 offset:10208
	v_fmac_f32_e32 v40, v51, v14
	v_fmac_f32_e32 v42, v50, v8
	v_fmac_f32_e32 v40, v56, v15
	v_fmac_f32_e32 v42, v44, v9
	v_fmac_f32_e32 v40, v54, v16
	s_waitcnt lgkmcnt(2)
	v_fmac_f32_e32 v42, v53, v10
	ds_read_b128 v[6:9], v19 offset:10224
	v_fmac_f32_e32 v40, v52, v17
	v_fmac_f32_e32 v42, v43, v11
	v_pk_mul_f32 v[10:11], v[30:31], v[12:13]
	s_waitcnt lgkmcnt(1)
	v_fmac_f32_e32 v40, v45, v82
	v_add_f32_e32 v10, v42, v10
	v_fmac_f32_e32 v40, v46, v83
	v_add_f32_e32 v12, v10, v11
	v_pk_mul_f32 v[10:11], v[34:35], v[84:85]
	v_pk_mul_f32 v[2:3], v[32:33], v[2:3]
	v_add_f32_e32 v10, v40, v10
	v_add_f32_e32 v2, v12, v2
	v_add_f32_e32 v10, v10, v11
	v_add_f32_e32 v11, v2, v3
	s_waitcnt lgkmcnt(0)
	v_pk_mul_f32 v[2:3], v[22:23], v[6:7]
	s_nop 0
	v_add_f32_e32 v2, v10, v2
	v_add_f32_e32 v6, v2, v3
	v_pk_mul_f32 v[2:3], v[20:21], v[4:5]
	v_cvt_pk_bf16_f32 v5, v64, v66
	v_add_f32_e32 v2, v11, v2
	v_add_f32_e32 v4, v2, v3
	v_pk_mul_f32 v[2:3], v[24:25], v[8:9]
	s_nop 0
	v_add_f32_e32 v2, v6, v2
	v_add_f32_e32 v2, v2, v3
	v_med3_f32 v2, v2, s5, v38
	v_mul_f32_e32 v2, 0x3fb8aa3b, v2
	v_exp_f32_e32 v10, v2
	v_med3_f32 v2, v4, s5, v38
	v_mul_f32_e32 v2, 0x3fb8aa3b, v2
	v_exp_f32_e32 v11, v2
	v_cvt_pk_bf16_f32 v2, v10, s0
	global_store_short v[28:29], v2, off offset:1920
	v_lshlrev_b32_e32 v2, 7, v36
	v_or3_b32 v26, v2, s4, v26
	v_lshl_add_u64 v[6:7], s[12:13], 0, v[26:27]
	v_cvt_pk_bf16_f32 v2, v37, v41
	v_cvt_pk_bf16_f32 v3, v48, v58
	v_cvt_pk_bf16_f32 v4, v60, v62
	global_store_dwordx4 v[6:7], v[2:5], off
	v_lshl_add_u64 v[8:9], s[14:15], 0, v[26:27]
	s_mov_b64 s[4:5], 0
	v_cvt_pk_bf16_f32 v2, v68, v70
	v_cvt_pk_bf16_f32 v3, v72, v74
	v_cvt_pk_bf16_f32 v4, v76, v78
	v_cvt_pk_bf16_f32 v5, v80, v11
	global_store_dwordx4 v[6:7], v[2:5], off offset:16
	s_nop 1
	v_cvt_pk_bf16_f32 v2, v18, v39
	v_cvt_pk_bf16_f32 v3, v47, v55
	v_cvt_pk_bf16_f32 v4, v59, v61
	v_cvt_pk_bf16_f32 v5, v63, v65
	global_store_dwordx4 v[8:9], v[2:5], off
	s_nop 1
	v_cvt_pk_bf16_f32 v2, v67, v69
	v_cvt_pk_bf16_f32 v3, v71, v73
	v_cvt_pk_bf16_f32 v4, v75, v77
	v_cvt_pk_bf16_f32 v5, v79, v10
	global_store_dwordx4 v[8:9], v[2:5], off offset:16

	.amdhsa_kernel _Z11prep_kernelPKfS0_S0_S0_S0_S0_S0_S0_S0_S0_S0_S0_PtS1_S1_S1_S1_S1_
		.amdhsa_group_segment_fixed_size 16640
		.amdhsa_private_segment_fixed_size 0
		.amdhsa_kernarg_size 144
		.amdhsa_user_sgpr_count 2
		.amdhsa_user_sgpr_dispatch_ptr 0
		.amdhsa_user_sgpr_queue_ptr 0
		.amdhsa_user_sgpr_kernarg_segment_ptr 1
		.amdhsa_user_sgpr_dispatch_id 0
		.amdhsa_user_sgpr_kernarg_preload_length 0
		.amdhsa_user_sgpr_kernarg_preload_offset 0
		.amdhsa_user_sgpr_private_segment_size 0
		.amdhsa_uses_dynamic_stack 0
		.amdhsa_enable_private_segment 0
		.amdhsa_system_sgpr_workgroup_id_x 1
		.amdhsa_system_sgpr_workgroup_id_y 0
		.amdhsa_system_sgpr_workgroup_id_z 0
		.amdhsa_system_sgpr_workgroup_info 0
		.amdhsa_system_vgpr_workitem_id 0
		.amdhsa_next_free_vgpr 164
		.amdhsa_next_free_sgpr 28
		.amdhsa_accum_offset 152
		.amdhsa_reserve_vcc 1
		.amdhsa_float_round_mode_32 0
		.amdhsa_float_round_mode_16_64 0
		.amdhsa_float_denorm_mode_32 3
		.amdhsa_float_denorm_mode_16_64 3
		.amdhsa_dx10_clamp 1
		.amdhsa_ieee_mode 1
		.amdhsa_fp16_overflow 0
		.amdhsa_tg_split 0
		.amdhsa_exception_fp_ieee_invalid_op 0
		.amdhsa_exception_fp_denorm_src 0
		.amdhsa_exception_fp_ieee_div_zero 0
		.amdhsa_exception_fp_ieee_overflow 0
		.amdhsa_exception_fp_ieee_underflow 0
		.amdhsa_exception_fp_ieee_inexact 0
		.amdhsa_exception_int_div_zero 0
	.end_amdhsa_kernel

amdhsa.kernels:
  - .agpr_count:     0
    .args:
      - .actual_access:  read_only
        .address_space:  global
        .offset:         0
        .size:           8
        .value_kind:     global_buffer
      - .actual_access:  read_only
        .address_space:  global
        .offset:         8
        .size:           8
        .value_kind:     global_buffer
      - .actual_access:  write_only
        .address_space:  global
        .offset:         16
        .size:           8
        .value_kind:     global_buffer
      - .offset:         24
        .size:           4
        .value_kind:     by_value
      - .offset:         28
        .size:           4
        .value_kind:     by_value
      - .offset:         32
        .size:           4
        .value_kind:     by_value
      - .offset:         36
        .size:           4
        .value_kind:     by_value
    .group_segment_fixed_size: 8256
    .kernarg_segment_align: 8
    .kernarg_segment_size: 40
    .language:       OpenCL C
    .language_version:
      - 2
      - 0
    .max_flat_workgroup_size: 256
    .name:           _Z14gemm_f32_naivePKfS0_Pfiiii
    .private_segment_fixed_size: 0
    .sgpr_count:     24
    .sgpr_spill_count: 0
    .symbol:         _Z14gemm_f32_naivePKfS0_Pfiiii.kd
    .uniform_work_group_size: 1
    .uses_dynamic_stack: false
    .vgpr_count:     76
    .vgpr_spill_count: 0
    .wavefront_size: 64
  - .agpr_count:     0
    .args:
      - .actual_access:  read_only
        .address_space:  global
        .offset:         0
        .size:           8
        .value_kind:     global_buffer
      - .actual_access:  write_only
        .address_space:  global
        .offset:         8
        .size:           8
        .value_kind:     global_buffer
      - .actual_access:  write_only
        .address_space:  global
        .offset:         16
        .size:           8
        .value_kind:     global_buffer
      - .actual_access:  write_only
        .address_space:  global
        .offset:         24
        .size:           8
        .value_kind:     global_buffer
      - .actual_access:  write_only
        .address_space:  global
        .offset:         32
        .size:           8
        .value_kind:     global_buffer
      - .actual_access:  write_only
        .address_space:  global
        .offset:         40
        .size:           8
        .value_kind:     global_buffer
      - .actual_access:  write_only
        .address_space:  global
        .offset:         48
        .size:           8
        .value_kind:     global_buffer
    .group_segment_fixed_size: 0
    .kernarg_segment_align: 8
    .kernarg_segment_size: 56
    .language:       OpenCL C
    .language_version:
      - 2
      - 0
    .max_flat_workgroup_size: 256
    .name:           _Z10post_naivePKfPtS1_S1_S1_S1_S1_
    .private_segment_fixed_size: 0
    .sgpr_count:     28
    .sgpr_spill_count: 0
    .symbol:         _Z10post_naivePKfPtS1_S1_S1_S1_S1_.kd
    .uniform_work_group_size: 1
    .uses_dynamic_stack: false
    .vgpr_count:     38
    .vgpr_spill_count: 0
    .wavefront_size: 64
  - .agpr_count:     0
    .args:
      - .actual_access:  read_only
        .address_space:  global
        .offset:         0
        .size:           8
        .value_kind:     global_buffer
      - .actual_access:  read_only
        .address_space:  global
        .offset:         8
        .size:           8
        .value_kind:     global_buffer
      - .actual_access:  read_only
        .address_space:  global
        .offset:         16
        .size:           8
        .value_kind:     global_buffer
      - .actual_access:  read_only
        .address_space:  global
        .offset:         24
        .size:           8
        .value_kind:     global_buffer
      - .actual_access:  read_only
        .address_space:  global
        .offset:         32
        .size:           8
        .value_kind:     global_buffer
      - .actual_access:  read_only
        .address_space:  global
        .offset:         40
        .size:           8
        .value_kind:     global_buffer
      - .actual_access:  read_only
        .address_space:  global
        .offset:         48
        .size:           8
        .value_kind:     global_buffer
      - .actual_access:  write_only
        .address_space:  global
        .offset:         56
        .size:           8
        .value_kind:     global_buffer
      - .actual_access:  write_only
        .address_space:  global
        .offset:         64
        .size:           8
        .value_kind:     global_buffer
      - .actual_access:  write_only
        .address_space:  global
        .offset:         72
        .size:           8
        .value_kind:     global_buffer
      - .actual_access:  write_only
        .address_space:  global
        .offset:         80
        .size:           8
        .value_kind:     global_buffer
    .group_segment_fixed_size: 1152
    .kernarg_segment_align: 8
    .kernarg_segment_size: 88
    .language:       OpenCL C
    .language_version:
      - 2
      - 0
    .max_flat_workgroup_size: 256
    .name:           _Z11gates_naivePKfS0_S0_S0_S0_S0_S0_PtS1_S1_S1_
    .private_segment_fixed_size: 0
    .sgpr_count:     32
    .sgpr_spill_count: 0
    .symbol:         _Z11gates_naivePKfS0_S0_S0_S0_S0_S0_PtS1_S1_S1_.kd
    .uniform_work_group_size: 1
    .uses_dynamic_stack: false
    .vgpr_count:     66
    .vgpr_spill_count: 0
    .wavefront_size: 64
  - .agpr_count:     0
    .args:
      - .actual_access:  read_only
        .address_space:  global
        .offset:         0
        .size:           8
        .value_kind:     global_buffer
      - .actual_access:  read_only
        .address_space:  global
        .offset:         8
        .size:           8
        .value_kind:     global_buffer
      - .actual_access:  read_only
        .address_space:  global
        .offset:         16
        .size:           8
        .value_kind:     global_buffer
      - .actual_access:  read_only
        .address_space:  global
        .offset:         24
        .size:           8
        .value_kind:     global_buffer
      - .actual_access:  read_only
        .address_space:  global
        .offset:         32
        .size:           8
        .value_kind:     global_buffer
      - .actual_access:  read_only
        .address_space:  global
        .offset:         40
        .size:           8
        .value_kind:     global_buffer
      - .actual_access:  read_only
        .address_space:  global
        .offset:         48
        .size:           8
        .value_kind:     global_buffer
      - .actual_access:  write_only
        .address_space:  global
        .offset:         56
        .size:           8
        .value_kind:     global_buffer
    .group_segment_fixed_size: 12560
    .kernarg_segment_align: 8
    .kernarg_segment_size: 64
    .language:       OpenCL C
    .language_version:
      - 2
      - 0
    .max_flat_workgroup_size: 256
    .name:           _Z10attn_naivePKtS0_S0_S0_S0_S0_PKfPf
    .private_segment_fixed_size: 0
    .sgpr_count:     33
    .sgpr_spill_count: 0
    .symbol:         _Z10attn_naivePKtS0_S0_S0_S0_S0_PKfPf.kd
    .uniform_work_group_size: 1
    .uses_dynamic_stack: false
    .vgpr_count:     82
    .vgpr_spill_count: 0
    .wavefront_size: 64
  - .agpr_count:     0
    .args:
      - .address_space:  global
        .offset:         0
        .size:           8
        .value_kind:     global_buffer
      - .address_space:  global
        .offset:         8
        .size:           8
        .value_kind:     global_buffer
      - .actual_access:  write_only
        .address_space:  global
        .offset:         16
        .size:           8
        .value_kind:     global_buffer
    .group_segment_fixed_size: 0
    .kernarg_segment_align: 8
    .kernarg_segment_size: 24
    .language:       OpenCL C
    .language_version:
      - 2
      - 0
    .max_flat_workgroup_size: 512
    .name:           _Z8gemm_outPKtS0_Pf
    .private_segment_fixed_size: 0
    .sgpr_count:     26
    .sgpr_spill_count: 0
    .symbol:         _Z8gemm_outPKtS0_Pf.kd
    .uniform_work_group_size: 1
    .uses_dynamic_stack: false
    .vgpr_count:     158
    .vgpr_spill_count: 0
    .wavefront_size: 64
  - .agpr_count:     0
    .args:
      - .address_space:  global
        .offset:         0
        .size:           8
        .value_kind:     global_buffer
      - .address_space:  global
        .offset:         8
        .size:           8
        .value_kind:     global_buffer
      - .actual_access:  write_only
        .address_space:  global
        .offset:         16
        .size:           8
        .value_kind:     global_buffer
    .group_segment_fixed_size: 0
    .kernarg_segment_align: 8
    .kernarg_segment_size: 24
    .language:       OpenCL C
    .language_version:
      - 2
      - 0
    .max_flat_workgroup_size: 512
    .name:           _Z9gemm_out2PKtS0_Pf
    .private_segment_fixed_size: 0
    .sgpr_count:     27
    .sgpr_spill_count: 0
    .symbol:         _Z9gemm_out2PKtS0_Pf.kd
    .uniform_work_group_size: 1
    .uses_dynamic_stack: false
    .vgpr_count:     146
    .vgpr_spill_count: 0
    .wavefront_size: 64
  - .agpr_count:     0
    .args:
      - .actual_access:  read_only
        .address_space:  global
        .offset:         0
        .size:           8
        .value_kind:     global_buffer
      - .actual_access:  write_only
        .address_space:  global
        .offset:         8
        .size:           8
        .value_kind:     global_buffer
    .group_segment_fixed_size: 0
    .kernarg_segment_align: 8
    .kernarg_segment_size: 16
    .language:       OpenCL C
    .language_version:
      - 2
      - 0
    .max_flat_workgroup_size: 256
    .name:           _Z6conv_xPKfPt
    .private_segment_fixed_size: 0
    .sgpr_count:     14
    .sgpr_spill_count: 0
    .symbol:         _Z6conv_xPKfPt.kd
    .uniform_work_group_size: 1
    .uses_dynamic_stack: false
    .vgpr_count:     12
    .vgpr_spill_count: 0
    .wavefront_size: 64
  - .agpr_count:     0
    .args:
      - .actual_access:  read_only
        .address_space:  global
        .offset:         0
        .size:           8
        .value_kind:     global_buffer
      - .actual_access:  read_only
        .address_space:  global
        .offset:         8
        .size:           8
        .value_kind:     global_buffer
      - .actual_access:  read_only
        .address_space:  global
        .offset:         16
        .size:           8
        .value_kind:     global_buffer
      - .actual_access:  read_only
        .address_space:  global
        .offset:         24
        .size:           8
        .value_kind:     global_buffer
      - .actual_access:  read_only
        .address_space:  global
        .offset:         32
        .size:           8
        .value_kind:     global_buffer
      - .actual_access:  write_only
        .address_space:  global
        .offset:         40
        .size:           8
        .value_kind:     global_buffer
      - .actual_access:  write_only
        .address_space:  global
        .offset:         48
        .size:           8
        .value_kind:     global_buffer
    .group_segment_fixed_size: 16640
    .kernarg_segment_align: 8
    .kernarg_segment_size: 56
    .language:       OpenCL C
    .language_version:
      - 2
      - 0
    .max_flat_workgroup_size: 256
    .name:           _Z7conv_wTPKfS0_S0_S0_S0_PtS1_
    .private_segment_fixed_size: 0
    .sgpr_count:     26
    .sgpr_spill_count: 0
    .symbol:         _Z7conv_wTPKfS0_S0_S0_S0_PtS1_.kd
    .uniform_work_group_size: 1
    .uses_dynamic_stack: false
    .vgpr_count:     51
    .vgpr_spill_count: 0
    .wavefront_size: 64
  - .agpr_count:     0
    .args:
      - .actual_access:  read_only
        .address_space:  global
        .offset:         0
        .size:           8
        .value_kind:     global_buffer
      - .actual_access:  read_only
        .address_space:  global
        .offset:         8
        .size:           8
        .value_kind:     global_buffer
      - .actual_access:  write_only
        .address_space:  global
        .offset:         16
        .size:           8
        .value_kind:     global_buffer
    .group_segment_fixed_size: 0
    .kernarg_segment_align: 8
    .kernarg_segment_size: 24
    .language:       OpenCL C
    .language_version:
      - 2
      - 0
    .max_flat_workgroup_size: 256
    .name:           _Z7conv_w1PKfS0_Pt
    .private_segment_fixed_size: 0
    .sgpr_count:     16
    .sgpr_spill_count: 0
    .symbol:         _Z7conv_w1PKfS0_Pt.kd
    .uniform_work_group_size: 1
    .uses_dynamic_stack: false
    .vgpr_count:     6
    .vgpr_spill_count: 0
    .wavefront_size: 64
  - .agpr_count:     8
    .args:
      - .actual_access:  read_only
        .address_space:  global
        .offset:         0
        .size:           8
        .value_kind:     global_buffer
      - .actual_access:  read_only
        .address_space:  global
        .offset:         8
        .size:           8
        .value_kind:     global_buffer
      - .actual_access:  read_only
        .address_space:  global
        .offset:         16
        .size:           8
        .value_kind:     global_buffer
      - .actual_access:  read_only
        .address_space:  global
        .offset:         24
        .size:           8
        .value_kind:     global_buffer
      - .actual_access:  read_only
        .address_space:  global
        .offset:         32
        .size:           8
        .value_kind:     global_buffer
      - .actual_access:  read_only
        .address_space:  global
        .offset:         40
        .size:           8
        .value_kind:     global_buffer
      - .actual_access:  write_only
        .address_space:  global
        .offset:         48
        .size:           8
        .value_kind:     global_buffer
      - .actual_access:  write_only
        .address_space:  global
        .offset:         56
        .size:           8
        .value_kind:     global_buffer
      - .actual_access:  write_only
        .address_space:  global
        .offset:         64
        .size:           8
        .value_kind:     global_buffer
    .group_segment_fixed_size: 10240
    .kernarg_segment_align: 8
    .kernarg_segment_size: 72
    .language:       OpenCL C
    .language_version:
      - 2
      - 0
    .max_flat_workgroup_size: 256
    .name:           _Z10gates_fastPKtS0_PKfS2_S2_S2_PtS3_S3_
    .private_segment_fixed_size: 0
    .sgpr_count:     24
    .sgpr_spill_count: 0
    .symbol:         _Z10gates_fastPKtS0_PKfS2_S2_S2_PtS3_S3_.kd
    .uniform_work_group_size: 1
    .uses_dynamic_stack: false
    .vgpr_count:     96
    .vgpr_spill_count: 0
    .wavefront_size: 64
  - .agpr_count:     4
    .args:
      - .actual_access:  read_only
        .address_space:  global
        .offset:         0
        .size:           8
        .value_kind:     global_buffer
      - .actual_access:  read_only
        .address_space:  global
        .offset:         8
        .size:           8
        .value_kind:     global_buffer
      - .actual_access:  read_only
        .address_space:  global
        .offset:         16
        .size:           8
        .value_kind:     global_buffer
      - .actual_access:  read_only
        .address_space:  global
        .offset:         24
        .size:           8
        .value_kind:     global_buffer
      - .actual_access:  write_only
        .address_space:  global
        .offset:         32
        .size:           8
        .value_kind:     global_buffer
      - .actual_access:  write_only
        .address_space:  global
        .offset:         40
        .size:           8
        .value_kind:     global_buffer
      - .actual_access:  write_only
        .address_space:  global
        .offset:         48
        .size:           8
        .value_kind:     global_buffer
    .group_segment_fixed_size: 0
    .kernarg_segment_align: 8
    .kernarg_segment_size: 56
    .language:       OpenCL C
    .language_version:
      - 2
      - 0
    .max_flat_workgroup_size: 256
    .name:           _Z10state_fastPKtS0_S0_S0_PtS1_Pf
    .private_segment_fixed_size: 0
    .sgpr_count:     20
    .sgpr_spill_count: 0
    .symbol:         _Z10state_fastPKtS0_S0_S0_PtS1_Pf.kd
    .uniform_work_group_size: 1
    .uses_dynamic_stack: false
    .vgpr_count:     184
    .vgpr_spill_count: 0
    .wavefront_size: 64
  - .agpr_count:     0
    .args:
      - .actual_access:  read_only
        .address_space:  global
        .offset:         0
        .size:           8
        .value_kind:     global_buffer
      - .actual_access:  read_only
        .address_space:  global
        .offset:         8
        .size:           8
        .value_kind:     global_buffer
      - .actual_access:  read_only
        .address_space:  global
        .offset:         16
        .size:           8
        .value_kind:     global_buffer
      - .actual_access:  write_only
        .address_space:  global
        .offset:         24
        .size:           8
        .value_kind:     global_buffer
      - .actual_access:  write_only
        .address_space:  global
        .offset:         32
        .size:           8
        .value_kind:     global_buffer
      - .actual_access:  write_only
        .address_space:  global
        .offset:         40
        .size:           8
        .value_kind:     global_buffer
    .group_segment_fixed_size: 0
    .kernarg_segment_align: 8
    .kernarg_segment_size: 48
    .language:       OpenCL C
    .language_version:
      - 2
      - 0
    .max_flat_workgroup_size: 256
    .name:           _Z11prefix_fastPKtS0_PKfPtS3_Pf
    .private_segment_fixed_size: 0
    .sgpr_count:     106
    .sgpr_spill_count: 41
    .symbol:         _Z11prefix_fastPKtS0_PKfPtS3_Pf.kd
    .uniform_work_group_size: 1
    .uses_dynamic_stack: false
    .vgpr_count:     205
    .vgpr_spill_count: 0
    .wavefront_size: 64
  - .agpr_count:     0
    .args:
      - .address_space:  global
        .offset:         0
        .size:           8
        .value_kind:     global_buffer
      - .address_space:  global
        .offset:         8
        .size:           8
        .value_kind:     global_buffer
      - .address_space:  global
        .offset:         16
        .size:           8
        .value_kind:     global_buffer
      - .actual_access:  read_only
        .address_space:  global
        .offset:         24
        .size:           8
        .value_kind:     global_buffer
      - .address_space:  global
        .offset:         32
        .size:           8
        .value_kind:     global_buffer
      - .address_space:  global
        .offset:         40
        .size:           8
        .value_kind:     global_buffer
      - .address_space:  global
        .offset:         48
        .size:           8
        .value_kind:     global_buffer
      - .address_space:  global
        .offset:         56
        .size:           8
        .value_kind:     global_buffer
      - .address_space:  global
        .offset:         64
        .size:           8
        .value_kind:     global_buffer
      - .address_space:  global
        .offset:         72
        .size:           8
        .value_kind:     global_buffer
      - .address_space:  global
        .offset:         80
        .size:           8
        .value_kind:     global_buffer
      - .actual_access:  write_only
        .address_space:  global
        .offset:         88
        .size:           8
        .value_kind:     global_buffer
    .group_segment_fixed_size: 0
    .kernarg_segment_align: 8
    .kernarg_segment_size: 96
    .language:       OpenCL C
    .language_version:
      - 2
      - 0
    .max_flat_workgroup_size: 512
    .name:           _Z9attn_fastPKtS0_S0_S0_S0_S0_S0_S0_S0_PKfS2_Pt
    .private_segment_fixed_size: 0
    .sgpr_count:     50
    .sgpr_spill_count: 0
    .symbol:         _Z9attn_fastPKtS0_S0_S0_S0_S0_S0_S0_S0_PKfS2_Pt.kd
    .uniform_work_group_size: 1
    .uses_dynamic_stack: false
    .vgpr_count:     152
    .vgpr_spill_count: 0
    .wavefront_size: 64
  - .agpr_count:     12
    .args:
      - .actual_access:  read_only
        .address_space:  global
        .offset:         0
        .size:           8
        .value_kind:     global_buffer
      - .actual_access:  read_only
        .address_space:  global
        .offset:         8
        .size:           8
        .value_kind:     global_buffer
      - .actual_access:  read_only
        .address_space:  global
        .offset:         16
        .size:           8
        .value_kind:     global_buffer
      - .actual_access:  read_only
        .address_space:  global
        .offset:         24
        .size:           8
        .value_kind:     global_buffer
      - .actual_access:  read_only
        .address_space:  global
        .offset:         32
        .size:           8
        .value_kind:     global_buffer
      - .actual_access:  read_only
        .address_space:  global
        .offset:         40
        .size:           8
        .value_kind:     global_buffer
      - .actual_access:  read_only
        .address_space:  global
        .offset:         48
        .size:           8
        .value_kind:     global_buffer
      - .actual_access:  read_only
        .address_space:  global
        .offset:         56
        .size:           8
        .value_kind:     global_buffer
      - .actual_access:  read_only
        .address_space:  global
        .offset:         64
        .size:           8
        .value_kind:     global_buffer
      - .actual_access:  read_only
        .address_space:  global
        .offset:         72
        .size:           8
        .value_kind:     global_buffer
      - .actual_access:  read_only
        .address_space:  global
        .offset:         80
        .size:           8
        .value_kind:     global_buffer
      - .actual_access:  read_only
        .address_space:  global
        .offset:         88
        .size:           8
        .value_kind:     global_buffer
      - .actual_access:  write_only
        .address_space:  global
        .offset:         96
        .size:           8
        .value_kind:     global_buffer
      - .actual_access:  write_only
        .address_space:  global
        .offset:         104
        .size:           8
        .value_kind:     global_buffer
      - .actual_access:  write_only
        .address_space:  global
        .offset:         112
        .size:           8
        .value_kind:     global_buffer
      - .actual_access:  write_only
        .address_space:  global
        .offset:         120
        .size:           8
        .value_kind:     global_buffer
      - .actual_access:  write_only
        .address_space:  global
        .offset:         128
        .size:           8
        .value_kind:     global_buffer
      - .actual_access:  write_only
        .address_space:  global
        .offset:         136
        .size:           8
        .value_kind:     global_buffer
    .group_segment_fixed_size: 16640
    .kernarg_segment_align: 8
    .kernarg_segment_size: 144
    .language:       OpenCL C
    .language_version:
      - 2
      - 0
    .max_flat_workgroup_size: 256
    .name:           _Z11prep_kernelPKfS0_S0_S0_S0_S0_S0_S0_S0_S0_S0_S0_PtS1_S1_S1_S1_S1_
    .private_segment_fixed_size: 0
    .sgpr_count:     34
    .sgpr_spill_count: 0
    .symbol:         _Z11prep_kernelPKfS0_S0_S0_S0_S0_S0_S0_S0_S0_S0_S0_PtS1_S1_S1_S1_S1_.kd
    .uniform_work_group_size: 1
    .uses_dynamic_stack: false
    .vgpr_count:     164
    .vgpr_spill_count: 0
    .wavefront_size: 64
  - .agpr_count:     0
    .args:
      - .address_space:  global
        .offset:         0
        .size:           8
        .value_kind:     global_buffer
      - .address_space:  global
        .offset:         8
        .size:           8
        .value_kind:     global_buffer
      - .offset:         16
        .size:           4
        .value_kind:     by_value
      - .offset:         20
        .size:           4
        .value_kind:     by_value
      - .offset:         24
        .size:           4
        .value_kind:     by_value
      - .offset:         28
        .size:           4
        .value_kind:     by_value
      - .address_space:  global
        .offset:         32
        .size:           8
        .value_kind:     global_buffer
    .group_segment_fixed_size: 0
    .kernarg_segment_align: 8
    .kernarg_segment_size: 40
    .language:       OpenCL C
    .language_version:
      - 2
      - 0
    .max_flat_workgroup_size: 1024
    .name:           _Z9dbg_cmp16PKtS0_iiffPf
    .private_segment_fixed_size: 0
    .sgpr_count:     18
    .sgpr_spill_count: 0
    .symbol:         _Z9dbg_cmp16PKtS0_iiffPf.kd
    .uniform_work_group_size: 1
    .uses_dynamic_stack: false
    .vgpr_count:     5
    .vgpr_spill_count: 0
    .wavefront_size: 64
  - .agpr_count:     0
    .args:
      - .address_space:  global
        .offset:         0
        .size:           8
        .value_kind:     global_buffer
      - .address_space:  global
        .offset:         8
        .size:           8
        .value_kind:     global_buffer
      - .offset:         16
        .size:           4
        .value_kind:     by_value
      - .offset:         20
        .size:           4
        .value_kind:     by_value
      - .offset:         24
        .size:           56
        .value_kind:     by_value
    .group_segment_fixed_size: 0
    .kernarg_segment_align: 8
    .kernarg_segment_size: 80
    .language:       OpenCL C
    .language_version:
      - 2
      - 0
    .max_flat_workgroup_size: 512
    .name:           _Z5gemm8ILi0EEvPKtS1_ii7EpiArgs
    .private_segment_fixed_size: 0
    .sgpr_count:     36
    .sgpr_spill_count: 0
    .symbol:         _Z5gemm8ILi0EEvPKtS1_ii7EpiArgs.kd
    .uniform_work_group_size: 1
    .uses_dynamic_stack: false
    .vgpr_count:     246
    .vgpr_spill_count: 0
    .wavefront_size: 64
  - .agpr_count:     0
    .args:
      - .address_space:  global
        .offset:         0
        .size:           8
        .value_kind:     global_buffer
      - .address_space:  global
        .offset:         8
        .size:           8
        .value_kind:     global_buffer
      - .address_space:  global
        .offset:         16
        .size:           8
        .value_kind:     global_buffer
      - .address_space:  global
        .offset:         24
        .size:           8
        .value_kind:     global_buffer
      - .actual_access:  write_only
        .address_space:  global
        .offset:         32
        .size:           8
        .value_kind:     global_buffer
      - .actual_access:  write_only
        .address_space:  global
        .offset:         40
        .size:           8
        .value_kind:     global_buffer
      - .actual_access:  write_only
        .address_space:  global
        .offset:         48
        .size:           8
        .value_kind:     global_buffer
    .group_segment_fixed_size: 81920
    .kernarg_segment_align: 8
    .kernarg_segment_size: 56
    .language:       OpenCL C
    .language_version:
      - 2
      - 0
    .max_flat_workgroup_size: 256
    .name:           _Z9scan_fastILb1EEvPKtS1_S1_S1_PtS2_Pf
    .private_segment_fixed_size: 0
    .sgpr_count:     62
    .sgpr_spill_count: 0
    .symbol:         _Z9scan_fastILb1EEvPKtS1_S1_S1_PtS2_Pf.kd
    .uniform_work_group_size: 1
    .uses_dynamic_stack: false
    .vgpr_count:     160
    .vgpr_spill_count: 0
    .wavefront_size: 64
